# router tails: xor-16 transposing exchange via v_permlane16_swap and xor-8 via DPP row_ror:8 (no ds_bpermute), on top of v86
# baseline (speedup 1.0000x reference)
; #define LAS __attribute__((address_space(3)))
; __device__ __forceinline__ void phase_norm2(const Params& p, const Ctx& F, const int l) {
;     ...
;         f32x2 lg[16];
;         unsigned wro = (unsigned)(uintptr_t)wr; asm volatile("" : "+v"(wro));
;         const LAS float* wr2 = (const LAS float*)(uintptr_t)wro;
; #pragma unroll
;         for (int e = 0; e < 16; ++e) { f32x2 a = {0.f, 0.f};
; #pragma unroll
;             for (int j = 0; j < 8; ++j) { const f32x4 w = *((const LAS f32x4*)(wr2 + e * DM) + F.lane + 64 * j);
; #pragma unroll
;                 for (int c = 0; c < 4; ++c) a += vv[j][c] * w[c]; }
;             lg[e] = a; }
.LBB0_937:
	s_or_b64 exec, exec, s[12:13]
	v_mov_b32_e32 v1, v35
	s_nop 0
	v_lshl_add_u32 v182, v132, 4, v1
	v_add_u32_e32 v244, 0x10000, v182
	ds_read_b128 v[224:227], v182
	ds_read_b128 v[228:231], v182 offset:1024
	ds_read_b128 v[232:235], v182 offset:2048
	ds_read_b128 v[236:239], v182 offset:3072
	s_waitcnt lgkmcnt(3)
	v_pk_fma_f32 v[156:157], v[124:125], v[224:225], 0 op_sel_hi:[1,0,0]
	s_nop 0
	v_pk_fma_f32 v[152:153], v[126:127], v[224:225], v[156:157] op_sel:[0,1,0]
	s_nop 0
	v_pk_fma_f32 v[152:153], v[128:129], v[226:227], v[152:153] op_sel_hi:[1,0,1]
	v_mov_b32_e32 v154, v227
	v_pk_fma_f32 v[156:157], v[130:131], v[154:155], v[152:153] op_sel_hi:[1,0,1]
	ds_read_b128 v[240:243], v182 offset:4096
	s_waitcnt lgkmcnt(3)
	v_pk_fma_f32 v[156:157], v[112:113], v[228:229], v[156:157] op_sel_hi:[1,0,1]
	s_nop 0
	v_pk_fma_f32 v[152:153], v[114:115], v[228:229], v[156:157] op_sel:[0,1,0]
	s_nop 0
	v_pk_fma_f32 v[152:153], v[118:119], v[230:231], v[152:153] op_sel_hi:[1,0,1]
	v_mov_b32_e32 v154, v231
	v_pk_fma_f32 v[156:157], v[122:123], v[154:155], v[152:153] op_sel_hi:[1,0,1]
	ds_read_b128 v[224:227], v182 offset:5120
	s_waitcnt lgkmcnt(3)
	v_pk_fma_f32 v[156:157], v[108:109], v[232:233], v[156:157] op_sel_hi:[1,0,1]
	s_nop 0
	v_pk_fma_f32 v[152:153], v[110:111], v[232:233], v[156:157] op_sel:[0,1,0]
	s_nop 0
	v_pk_fma_f32 v[152:153], v[116:117], v[234:235], v[152:153] op_sel_hi:[1,0,1]
	v_mov_b32_e32 v154, v235
	v_pk_fma_f32 v[156:157], v[120:121], v[154:155], v[152:153] op_sel_hi:[1,0,1]
	ds_read_b128 v[228:231], v182 offset:6144
	s_waitcnt lgkmcnt(3)
	v_pk_fma_f32 v[156:157], v[96:97], v[236:237], v[156:157] op_sel_hi:[1,0,1]
	s_nop 0
	v_pk_fma_f32 v[152:153], v[98:99], v[236:237], v[156:157] op_sel:[0,1,0]
	s_nop 0
	v_pk_fma_f32 v[152:153], v[102:103], v[238:239], v[152:153] op_sel_hi:[1,0,1]
	v_mov_b32_e32 v154, v239
	v_pk_fma_f32 v[156:157], v[106:107], v[154:155], v[152:153] op_sel_hi:[1,0,1]
	ds_read_b128 v[232:235], v182 offset:7168
	s_waitcnt lgkmcnt(3)
	v_pk_fma_f32 v[156:157], v[92:93], v[240:241], v[156:157] op_sel_hi:[1,0,1]
	s_nop 0
	v_pk_fma_f32 v[152:153], v[94:95], v[240:241], v[156:157] op_sel:[0,1,0]
	s_nop 0
	v_pk_fma_f32 v[152:153], v[100:101], v[242:243], v[152:153] op_sel_hi:[1,0,1]
	v_mov_b32_e32 v154, v243
	v_pk_fma_f32 v[156:157], v[104:105], v[154:155], v[152:153] op_sel_hi:[1,0,1]
	ds_read_b128 v[236:239], v182 offset:8192
	s_waitcnt lgkmcnt(3)
	v_pk_fma_f32 v[156:157], v[80:81], v[224:225], v[156:157] op_sel_hi:[1,0,1]
	s_nop 0
	v_pk_fma_f32 v[152:153], v[82:83], v[224:225], v[156:157] op_sel:[0,1,0]
	s_nop 0
	v_pk_fma_f32 v[152:153], v[86:87], v[226:227], v[152:153] op_sel_hi:[1,0,1]
	v_mov_b32_e32 v154, v227
	v_pk_fma_f32 v[156:157], v[90:91], v[154:155], v[152:153] op_sel_hi:[1,0,1]
	ds_read_b128 v[240:243], v182 offset:9216
	s_waitcnt lgkmcnt(3)
	v_pk_fma_f32 v[156:157], v[76:77], v[228:229], v[156:157] op_sel_hi:[1,0,1]
	s_nop 0
	v_pk_fma_f32 v[152:153], v[78:79], v[228:229], v[156:157] op_sel:[0,1,0]
	s_nop 0
	v_pk_fma_f32 v[152:153], v[84:85], v[230:231], v[152:153] op_sel_hi:[1,0,1]
	v_mov_b32_e32 v154, v231
	v_pk_fma_f32 v[156:157], v[88:89], v[154:155], v[152:153] op_sel_hi:[1,0,1]
	ds_read_b128 v[224:227], v182 offset:10240
	s_waitcnt lgkmcnt(3)
	v_pk_fma_f32 v[156:157], v[68:69], v[232:233], v[156:157] op_sel_hi:[1,0,1]
	s_nop 0
	v_pk_fma_f32 v[152:153], v[70:71], v[232:233], v[156:157] op_sel:[0,1,0]
	s_nop 0
	v_pk_fma_f32 v[152:153], v[72:73], v[234:235], v[152:153] op_sel_hi:[1,0,1]
	v_mov_b32_e32 v154, v235
	v_pk_fma_f32 v[152:153], v[74:75], v[154:155], v[152:153] op_sel_hi:[1,0,1]
	ds_read_b128 v[228:231], v182 offset:11264
	s_waitcnt lgkmcnt(3)
	v_pk_fma_f32 v[158:159], v[124:125], v[236:237], 0 op_sel_hi:[1,0,0]
	s_nop 0
	v_pk_fma_f32 v[154:155], v[126:127], v[236:237], v[158:159] op_sel:[0,1,0]
	s_nop 0
	v_pk_fma_f32 v[154:155], v[128:129], v[238:239], v[154:155] op_sel_hi:[1,0,1]
	v_mov_b32_e32 v156, v239
	v_pk_fma_f32 v[158:159], v[130:131], v[156:157], v[154:155] op_sel_hi:[1,0,1]
	ds_read_b128 v[232:235], v182 offset:12288
	s_waitcnt lgkmcnt(3)
	v_pk_fma_f32 v[158:159], v[112:113], v[240:241], v[158:159] op_sel_hi:[1,0,1]
	s_nop 0
	v_pk_fma_f32 v[154:155], v[114:115], v[240:241], v[158:159] op_sel:[0,1,0]
	s_nop 0
	v_pk_fma_f32 v[154:155], v[118:119], v[242:243], v[154:155] op_sel_hi:[1,0,1]
	v_mov_b32_e32 v156, v243
	v_pk_fma_f32 v[158:159], v[122:123], v[156:157], v[154:155] op_sel_hi:[1,0,1]
	ds_read_b128 v[236:239], v182 offset:13312
	s_waitcnt lgkmcnt(3)
	v_pk_fma_f32 v[158:159], v[108:109], v[224:225], v[158:159] op_sel_hi:[1,0,1]
	s_nop 0
	v_pk_fma_f32 v[154:155], v[110:111], v[224:225], v[158:159] op_sel:[0,1,0]
	s_nop 0
	v_pk_fma_f32 v[154:155], v[116:117], v[226:227], v[154:155] op_sel_hi:[1,0,1]
	v_mov_b32_e32 v156, v227
	v_pk_fma_f32 v[158:159], v[120:121], v[156:157], v[154:155] op_sel_hi:[1,0,1]
	ds_read_b128 v[240:243], v182 offset:14336
	s_waitcnt lgkmcnt(3)
	v_pk_fma_f32 v[158:159], v[96:97], v[228:229], v[158:159] op_sel_hi:[1,0,1]
	s_nop 0
	v_pk_fma_f32 v[154:155], v[98:99], v[228:229], v[158:159] op_sel:[0,1,0]
	s_nop 0
	v_pk_fma_f32 v[154:155], v[102:103], v[230:231], v[154:155] op_sel_hi:[1,0,1]
	v_mov_b32_e32 v156, v231
	v_pk_fma_f32 v[158:159], v[106:107], v[156:157], v[154:155] op_sel_hi:[1,0,1]
	ds_read_b128 v[224:227], v182 offset:15360
	s_waitcnt lgkmcnt(3)
	v_pk_fma_f32 v[158:159], v[92:93], v[232:233], v[158:159] op_sel_hi:[1,0,1]
	s_nop 0
	v_pk_fma_f32 v[154:155], v[94:95], v[232:233], v[158:159] op_sel:[0,1,0]
	s_nop 0
	v_pk_fma_f32 v[154:155], v[100:101], v[234:235], v[154:155] op_sel_hi:[1,0,1]
	v_mov_b32_e32 v156, v235
	v_pk_fma_f32 v[158:159], v[104:105], v[156:157], v[154:155] op_sel_hi:[1,0,1]
	ds_read_b128 v[228:231], v182 offset:16384
	s_waitcnt lgkmcnt(3)
; #define LAS __attribute__((address_space(3)))
; __device__ __forceinline__ void phase_norm2(const Params& p, const Ctx& F, const int l) {
;     ...
; #pragma unroll
;         for (int e = 0; e < 16; ++e) { f32x2 a = {0.f, 0.f};
; #pragma unroll
;             for (int j = 0; j < 8; ++j) { const f32x4 w = *((const LAS f32x4*)(wr2 + e * DM) + F.lane + 64 * j);
; #pragma unroll
;                 for (int c = 0; c < 4; ++c) a += vv[j][c] * w[c]; }
;             lg[e] = a; }
	v_pk_fma_f32 v[158:159], v[80:81], v[236:237], v[158:159] op_sel_hi:[1,0,1]
	s_nop 0
	v_pk_fma_f32 v[154:155], v[82:83], v[236:237], v[158:159] op_sel:[0,1,0]
	s_nop 0
	v_pk_fma_f32 v[154:155], v[86:87], v[238:239], v[154:155] op_sel_hi:[1,0,1]
	v_mov_b32_e32 v156, v239
	v_pk_fma_f32 v[158:159], v[90:91], v[156:157], v[154:155] op_sel_hi:[1,0,1]
	ds_read_b128 v[232:235], v182 offset:17408
	s_waitcnt lgkmcnt(3)
	v_pk_fma_f32 v[158:159], v[76:77], v[240:241], v[158:159] op_sel_hi:[1,0,1]
	s_nop 0
	v_pk_fma_f32 v[154:155], v[78:79], v[240:241], v[158:159] op_sel:[0,1,0]
	s_nop 0
	v_pk_fma_f32 v[154:155], v[84:85], v[242:243], v[154:155] op_sel_hi:[1,0,1]
	v_mov_b32_e32 v156, v243
	v_pk_fma_f32 v[158:159], v[88:89], v[156:157], v[154:155] op_sel_hi:[1,0,1]
	ds_read_b128 v[236:239], v182 offset:18432
	s_waitcnt lgkmcnt(3)
	v_pk_fma_f32 v[158:159], v[68:69], v[224:225], v[158:159] op_sel_hi:[1,0,1]
	s_nop 0
	v_pk_fma_f32 v[154:155], v[70:71], v[224:225], v[158:159] op_sel:[0,1,0]
	s_nop 0
	v_pk_fma_f32 v[154:155], v[72:73], v[226:227], v[154:155] op_sel_hi:[1,0,1]
	v_mov_b32_e32 v156, v227
	v_pk_fma_f32 v[154:155], v[74:75], v[156:157], v[154:155] op_sel_hi:[1,0,1]
	ds_read_b128 v[240:243], v182 offset:19456
	s_waitcnt lgkmcnt(3)
	v_pk_fma_f32 v[160:161], v[124:125], v[228:229], 0 op_sel_hi:[1,0,0]
	s_nop 0
	v_pk_fma_f32 v[156:157], v[126:127], v[228:229], v[160:161] op_sel:[0,1,0]
	s_nop 0
	v_pk_fma_f32 v[156:157], v[128:129], v[230:231], v[156:157] op_sel_hi:[1,0,1]
	v_mov_b32_e32 v158, v231
	v_pk_fma_f32 v[160:161], v[130:131], v[158:159], v[156:157] op_sel_hi:[1,0,1]
	ds_read_b128 v[224:227], v182 offset:20480
	s_waitcnt lgkmcnt(3)
	v_pk_fma_f32 v[160:161], v[112:113], v[232:233], v[160:161] op_sel_hi:[1,0,1]
	s_nop 0
	v_pk_fma_f32 v[156:157], v[114:115], v[232:233], v[160:161] op_sel:[0,1,0]
	s_nop 0
	v_pk_fma_f32 v[156:157], v[118:119], v[234:235], v[156:157] op_sel_hi:[1,0,1]
	v_mov_b32_e32 v158, v235
	v_pk_fma_f32 v[160:161], v[122:123], v[158:159], v[156:157] op_sel_hi:[1,0,1]
	ds_read_b128 v[228:231], v182 offset:21504
	s_waitcnt lgkmcnt(3)
	v_pk_fma_f32 v[160:161], v[108:109], v[236:237], v[160:161] op_sel_hi:[1,0,1]
	s_nop 0
	v_pk_fma_f32 v[156:157], v[110:111], v[236:237], v[160:161] op_sel:[0,1,0]
	s_nop 0
	v_pk_fma_f32 v[156:157], v[116:117], v[238:239], v[156:157] op_sel_hi:[1,0,1]
	v_mov_b32_e32 v158, v239
	v_pk_fma_f32 v[160:161], v[120:121], v[158:159], v[156:157] op_sel_hi:[1,0,1]
	ds_read_b128 v[232:235], v182 offset:22528
	s_waitcnt lgkmcnt(3)
	v_pk_fma_f32 v[160:161], v[96:97], v[240:241], v[160:161] op_sel_hi:[1,0,1]
	s_nop 0
	v_pk_fma_f32 v[156:157], v[98:99], v[240:241], v[160:161] op_sel:[0,1,0]
	s_nop 0
	v_pk_fma_f32 v[156:157], v[102:103], v[242:243], v[156:157] op_sel_hi:[1,0,1]
	v_mov_b32_e32 v158, v243
	v_pk_fma_f32 v[160:161], v[106:107], v[158:159], v[156:157] op_sel_hi:[1,0,1]
	ds_read_b128 v[236:239], v182 offset:23552
	s_waitcnt lgkmcnt(3)
	v_pk_fma_f32 v[160:161], v[92:93], v[224:225], v[160:161] op_sel_hi:[1,0,1]
	s_nop 0
	v_pk_fma_f32 v[156:157], v[94:95], v[224:225], v[160:161] op_sel:[0,1,0]
	s_nop 0
	v_pk_fma_f32 v[156:157], v[100:101], v[226:227], v[156:157] op_sel_hi:[1,0,1]
	v_mov_b32_e32 v158, v227
	v_pk_fma_f32 v[160:161], v[104:105], v[158:159], v[156:157] op_sel_hi:[1,0,1]
	ds_read_b128 v[240:243], v182 offset:24576
	s_waitcnt lgkmcnt(3)
	v_pk_fma_f32 v[160:161], v[80:81], v[228:229], v[160:161] op_sel_hi:[1,0,1]
	s_nop 0
	v_pk_fma_f32 v[156:157], v[82:83], v[228:229], v[160:161] op_sel:[0,1,0]
	s_nop 0
	v_pk_fma_f32 v[156:157], v[86:87], v[230:231], v[156:157] op_sel_hi:[1,0,1]
	v_mov_b32_e32 v158, v231
	v_pk_fma_f32 v[160:161], v[90:91], v[158:159], v[156:157] op_sel_hi:[1,0,1]
	ds_read_b128 v[224:227], v182 offset:25600
	s_waitcnt lgkmcnt(3)
	v_pk_fma_f32 v[160:161], v[76:77], v[232:233], v[160:161] op_sel_hi:[1,0,1]
	s_nop 0
	v_pk_fma_f32 v[156:157], v[78:79], v[232:233], v[160:161] op_sel:[0,1,0]
	s_nop 0
	v_pk_fma_f32 v[156:157], v[84:85], v[234:235], v[156:157] op_sel_hi:[1,0,1]
	v_mov_b32_e32 v158, v235
	v_pk_fma_f32 v[160:161], v[88:89], v[158:159], v[156:157] op_sel_hi:[1,0,1]
	ds_read_b128 v[228:231], v182 offset:26624
	s_waitcnt lgkmcnt(3)
	v_pk_fma_f32 v[160:161], v[68:69], v[236:237], v[160:161] op_sel_hi:[1,0,1]
	s_nop 0
	v_pk_fma_f32 v[156:157], v[70:71], v[236:237], v[160:161] op_sel:[0,1,0]
	s_nop 0
	v_pk_fma_f32 v[156:157], v[72:73], v[238:239], v[156:157] op_sel_hi:[1,0,1]
	v_mov_b32_e32 v158, v239
	v_pk_fma_f32 v[156:157], v[74:75], v[158:159], v[156:157] op_sel_hi:[1,0,1]
	ds_read_b128 v[232:235], v182 offset:27648
	s_waitcnt lgkmcnt(3)
	v_pk_fma_f32 v[162:163], v[124:125], v[240:241], 0 op_sel_hi:[1,0,0]
	s_nop 0
	v_pk_fma_f32 v[158:159], v[126:127], v[240:241], v[162:163] op_sel:[0,1,0]
	s_nop 0
	v_pk_fma_f32 v[158:159], v[128:129], v[242:243], v[158:159] op_sel_hi:[1,0,1]
	v_mov_b32_e32 v160, v243
	v_pk_fma_f32 v[162:163], v[130:131], v[160:161], v[158:159] op_sel_hi:[1,0,1]
	ds_read_b128 v[236:239], v182 offset:28672
	s_waitcnt lgkmcnt(3)
	v_pk_fma_f32 v[162:163], v[112:113], v[224:225], v[162:163] op_sel_hi:[1,0,1]
	s_nop 0
	v_pk_fma_f32 v[158:159], v[114:115], v[224:225], v[162:163] op_sel:[0,1,0]
	s_nop 0
	v_pk_fma_f32 v[158:159], v[118:119], v[226:227], v[158:159] op_sel_hi:[1,0,1]
	v_mov_b32_e32 v160, v227
	v_pk_fma_f32 v[162:163], v[122:123], v[160:161], v[158:159] op_sel_hi:[1,0,1]
	ds_read_b128 v[240:243], v182 offset:29696
	s_waitcnt lgkmcnt(3)
	v_pk_fma_f32 v[162:163], v[108:109], v[228:229], v[162:163] op_sel_hi:[1,0,1]
	s_nop 0
	v_pk_fma_f32 v[158:159], v[110:111], v[228:229], v[162:163] op_sel:[0,1,0]
	s_nop 0
	v_pk_fma_f32 v[158:159], v[116:117], v[230:231], v[158:159] op_sel_hi:[1,0,1]
	v_mov_b32_e32 v160, v231
	v_pk_fma_f32 v[162:163], v[120:121], v[160:161], v[158:159] op_sel_hi:[1,0,1]
	ds_read_b128 v[224:227], v182 offset:30720
	s_waitcnt lgkmcnt(3)
; #define LAS __attribute__((address_space(3)))
; __device__ __forceinline__ void phase_norm2(const Params& p, const Ctx& F, const int l) {
;     ...
; #pragma unroll
;         for (int e = 0; e < 16; ++e) { f32x2 a = {0.f, 0.f};
; #pragma unroll
;             for (int j = 0; j < 8; ++j) { const f32x4 w = *((const LAS f32x4*)(wr2 + e * DM) + F.lane + 64 * j);
; #pragma unroll
;                 for (int c = 0; c < 4; ++c) a += vv[j][c] * w[c]; }
;             lg[e] = a; }
	v_pk_fma_f32 v[162:163], v[96:97], v[232:233], v[162:163] op_sel_hi:[1,0,1]
	s_nop 0
	v_pk_fma_f32 v[158:159], v[98:99], v[232:233], v[162:163] op_sel:[0,1,0]
	s_nop 0
	v_pk_fma_f32 v[158:159], v[102:103], v[234:235], v[158:159] op_sel_hi:[1,0,1]
	v_mov_b32_e32 v160, v235
	v_pk_fma_f32 v[162:163], v[106:107], v[160:161], v[158:159] op_sel_hi:[1,0,1]
	ds_read_b128 v[228:231], v182 offset:31744
	s_waitcnt lgkmcnt(3)
	v_pk_fma_f32 v[162:163], v[92:93], v[236:237], v[162:163] op_sel_hi:[1,0,1]
	s_nop 0
	v_pk_fma_f32 v[158:159], v[94:95], v[236:237], v[162:163] op_sel:[0,1,0]
	s_nop 0
	v_pk_fma_f32 v[158:159], v[100:101], v[238:239], v[158:159] op_sel_hi:[1,0,1]
	v_mov_b32_e32 v160, v239
	v_pk_fma_f32 v[162:163], v[104:105], v[160:161], v[158:159] op_sel_hi:[1,0,1]
	ds_read_b128 v[232:235], v182 offset:32768
	s_waitcnt lgkmcnt(3)
	v_pk_fma_f32 v[162:163], v[80:81], v[240:241], v[162:163] op_sel_hi:[1,0,1]
	s_nop 0
	v_pk_fma_f32 v[158:159], v[82:83], v[240:241], v[162:163] op_sel:[0,1,0]
	s_nop 0
	v_pk_fma_f32 v[158:159], v[86:87], v[242:243], v[158:159] op_sel_hi:[1,0,1]
	v_mov_b32_e32 v160, v243
	v_pk_fma_f32 v[162:163], v[90:91], v[160:161], v[158:159] op_sel_hi:[1,0,1]
	ds_read_b128 v[236:239], v182 offset:33792
	s_waitcnt lgkmcnt(3)
	v_pk_fma_f32 v[162:163], v[76:77], v[224:225], v[162:163] op_sel_hi:[1,0,1]
	s_nop 0
	v_pk_fma_f32 v[158:159], v[78:79], v[224:225], v[162:163] op_sel:[0,1,0]
	s_nop 0
	v_pk_fma_f32 v[158:159], v[84:85], v[226:227], v[158:159] op_sel_hi:[1,0,1]
	v_mov_b32_e32 v160, v227
	v_pk_fma_f32 v[162:163], v[88:89], v[160:161], v[158:159] op_sel_hi:[1,0,1]
	ds_read_b128 v[240:243], v182 offset:34816
	s_waitcnt lgkmcnt(3)
	v_pk_fma_f32 v[162:163], v[68:69], v[228:229], v[162:163] op_sel_hi:[1,0,1]
	s_nop 0
	v_pk_fma_f32 v[158:159], v[70:71], v[228:229], v[162:163] op_sel:[0,1,0]
	s_nop 0
	v_pk_fma_f32 v[158:159], v[72:73], v[230:231], v[158:159] op_sel_hi:[1,0,1]
	v_mov_b32_e32 v160, v231
	v_pk_fma_f32 v[158:159], v[74:75], v[160:161], v[158:159] op_sel_hi:[1,0,1]
	ds_read_b128 v[224:227], v182 offset:35840
	s_waitcnt lgkmcnt(3)
	v_pk_fma_f32 v[164:165], v[124:125], v[232:233], 0 op_sel_hi:[1,0,0]
	s_nop 0
	v_pk_fma_f32 v[160:161], v[126:127], v[232:233], v[164:165] op_sel:[0,1,0]
	s_nop 0
	v_pk_fma_f32 v[160:161], v[128:129], v[234:235], v[160:161] op_sel_hi:[1,0,1]
	v_mov_b32_e32 v162, v235
	v_pk_fma_f32 v[164:165], v[130:131], v[162:163], v[160:161] op_sel_hi:[1,0,1]
	ds_read_b128 v[228:231], v182 offset:36864
	s_waitcnt lgkmcnt(3)
	v_pk_fma_f32 v[164:165], v[112:113], v[236:237], v[164:165] op_sel_hi:[1,0,1]
	s_nop 0
	v_pk_fma_f32 v[160:161], v[114:115], v[236:237], v[164:165] op_sel:[0,1,0]
	s_nop 0
	v_pk_fma_f32 v[160:161], v[118:119], v[238:239], v[160:161] op_sel_hi:[1,0,1]
	v_mov_b32_e32 v162, v239
	v_pk_fma_f32 v[164:165], v[122:123], v[162:163], v[160:161] op_sel_hi:[1,0,1]
	ds_read_b128 v[232:235], v182 offset:37888
	s_waitcnt lgkmcnt(3)
	v_pk_fma_f32 v[164:165], v[108:109], v[240:241], v[164:165] op_sel_hi:[1,0,1]
	s_nop 0
	v_pk_fma_f32 v[160:161], v[110:111], v[240:241], v[164:165] op_sel:[0,1,0]
	s_nop 0
	v_pk_fma_f32 v[160:161], v[116:117], v[242:243], v[160:161] op_sel_hi:[1,0,1]
	v_mov_b32_e32 v162, v243
	v_pk_fma_f32 v[164:165], v[120:121], v[162:163], v[160:161] op_sel_hi:[1,0,1]
	ds_read_b128 v[236:239], v182 offset:38912
	s_waitcnt lgkmcnt(3)
	v_pk_fma_f32 v[164:165], v[96:97], v[224:225], v[164:165] op_sel_hi:[1,0,1]
	s_nop 0
	v_pk_fma_f32 v[160:161], v[98:99], v[224:225], v[164:165] op_sel:[0,1,0]
	s_nop 0
	v_pk_fma_f32 v[160:161], v[102:103], v[226:227], v[160:161] op_sel_hi:[1,0,1]
	v_mov_b32_e32 v162, v227
	v_pk_fma_f32 v[164:165], v[106:107], v[162:163], v[160:161] op_sel_hi:[1,0,1]
	ds_read_b128 v[240:243], v182 offset:39936
	s_waitcnt lgkmcnt(3)
	v_pk_fma_f32 v[164:165], v[92:93], v[228:229], v[164:165] op_sel_hi:[1,0,1]
	s_nop 0
	v_pk_fma_f32 v[160:161], v[94:95], v[228:229], v[164:165] op_sel:[0,1,0]
	s_nop 0
	v_pk_fma_f32 v[160:161], v[100:101], v[230:231], v[160:161] op_sel_hi:[1,0,1]
	v_mov_b32_e32 v162, v231
	v_pk_fma_f32 v[164:165], v[104:105], v[162:163], v[160:161] op_sel_hi:[1,0,1]
	ds_read_b128 v[224:227], v182 offset:40960
	s_waitcnt lgkmcnt(3)
	v_pk_fma_f32 v[164:165], v[80:81], v[232:233], v[164:165] op_sel_hi:[1,0,1]
	s_nop 0
	v_pk_fma_f32 v[160:161], v[82:83], v[232:233], v[164:165] op_sel:[0,1,0]
	s_nop 0
	v_pk_fma_f32 v[160:161], v[86:87], v[234:235], v[160:161] op_sel_hi:[1,0,1]
	v_mov_b32_e32 v162, v235
	v_pk_fma_f32 v[164:165], v[90:91], v[162:163], v[160:161] op_sel_hi:[1,0,1]
	ds_read_b128 v[228:231], v182 offset:41984
	s_waitcnt lgkmcnt(3)
	v_pk_fma_f32 v[164:165], v[76:77], v[236:237], v[164:165] op_sel_hi:[1,0,1]
	s_nop 0
	v_pk_fma_f32 v[160:161], v[78:79], v[236:237], v[164:165] op_sel:[0,1,0]
	s_nop 0
	v_pk_fma_f32 v[160:161], v[84:85], v[238:239], v[160:161] op_sel_hi:[1,0,1]
	v_mov_b32_e32 v162, v239
	v_pk_fma_f32 v[164:165], v[88:89], v[162:163], v[160:161] op_sel_hi:[1,0,1]
	ds_read_b128 v[232:235], v182 offset:43008
	s_waitcnt lgkmcnt(3)
	v_pk_fma_f32 v[164:165], v[68:69], v[240:241], v[164:165] op_sel_hi:[1,0,1]
	s_nop 0
	v_pk_fma_f32 v[160:161], v[70:71], v[240:241], v[164:165] op_sel:[0,1,0]
	s_nop 0
	v_pk_fma_f32 v[160:161], v[72:73], v[242:243], v[160:161] op_sel_hi:[1,0,1]
	v_mov_b32_e32 v162, v243
	v_pk_fma_f32 v[160:161], v[74:75], v[162:163], v[160:161] op_sel_hi:[1,0,1]
	ds_read_b128 v[236:239], v182 offset:44032
	s_waitcnt lgkmcnt(3)
	v_pk_fma_f32 v[166:167], v[124:125], v[224:225], 0 op_sel_hi:[1,0,0]
	s_nop 0
	v_pk_fma_f32 v[162:163], v[126:127], v[224:225], v[166:167] op_sel:[0,1,0]
	s_nop 0
	v_pk_fma_f32 v[162:163], v[128:129], v[226:227], v[162:163] op_sel_hi:[1,0,1]
	v_mov_b32_e32 v164, v227
	v_pk_fma_f32 v[166:167], v[130:131], v[164:165], v[162:163] op_sel_hi:[1,0,1]
	ds_read_b128 v[240:243], v182 offset:45056
	s_waitcnt lgkmcnt(3)
; #define LAS __attribute__((address_space(3)))
; __device__ __forceinline__ void phase_norm2(const Params& p, const Ctx& F, const int l) {
;     ...
; #pragma unroll
;         for (int e = 0; e < 16; ++e) { f32x2 a = {0.f, 0.f};
; #pragma unroll
;             for (int j = 0; j < 8; ++j) { const f32x4 w = *((const LAS f32x4*)(wr2 + e * DM) + F.lane + 64 * j);
; #pragma unroll
;                 for (int c = 0; c < 4; ++c) a += vv[j][c] * w[c]; }
;             lg[e] = a; }
	v_pk_fma_f32 v[166:167], v[112:113], v[228:229], v[166:167] op_sel_hi:[1,0,1]
	s_nop 0
	v_pk_fma_f32 v[162:163], v[114:115], v[228:229], v[166:167] op_sel:[0,1,0]
	s_nop 0
	v_pk_fma_f32 v[162:163], v[118:119], v[230:231], v[162:163] op_sel_hi:[1,0,1]
	v_mov_b32_e32 v164, v231
	v_pk_fma_f32 v[166:167], v[122:123], v[164:165], v[162:163] op_sel_hi:[1,0,1]
	ds_read_b128 v[224:227], v182 offset:46080
	s_waitcnt lgkmcnt(3)
	v_pk_fma_f32 v[166:167], v[108:109], v[232:233], v[166:167] op_sel_hi:[1,0,1]
	s_nop 0
	v_pk_fma_f32 v[162:163], v[110:111], v[232:233], v[166:167] op_sel:[0,1,0]
	s_nop 0
	v_pk_fma_f32 v[162:163], v[116:117], v[234:235], v[162:163] op_sel_hi:[1,0,1]
	v_mov_b32_e32 v164, v235
	v_pk_fma_f32 v[166:167], v[120:121], v[164:165], v[162:163] op_sel_hi:[1,0,1]
	ds_read_b128 v[228:231], v182 offset:47104
	s_waitcnt lgkmcnt(3)
	v_pk_fma_f32 v[166:167], v[96:97], v[236:237], v[166:167] op_sel_hi:[1,0,1]
	s_nop 0
	v_pk_fma_f32 v[162:163], v[98:99], v[236:237], v[166:167] op_sel:[0,1,0]
	s_nop 0
	v_pk_fma_f32 v[162:163], v[102:103], v[238:239], v[162:163] op_sel_hi:[1,0,1]
	v_mov_b32_e32 v164, v239
	v_pk_fma_f32 v[166:167], v[106:107], v[164:165], v[162:163] op_sel_hi:[1,0,1]
	ds_read_b128 v[232:235], v182 offset:48128
	s_waitcnt lgkmcnt(3)
	v_pk_fma_f32 v[166:167], v[92:93], v[240:241], v[166:167] op_sel_hi:[1,0,1]
	s_nop 0
	v_pk_fma_f32 v[162:163], v[94:95], v[240:241], v[166:167] op_sel:[0,1,0]
	s_nop 0
	v_pk_fma_f32 v[162:163], v[100:101], v[242:243], v[162:163] op_sel_hi:[1,0,1]
	v_mov_b32_e32 v164, v243
	v_pk_fma_f32 v[166:167], v[104:105], v[164:165], v[162:163] op_sel_hi:[1,0,1]
	ds_read_b128 v[236:239], v182 offset:49152
	s_waitcnt lgkmcnt(3)
	v_pk_fma_f32 v[166:167], v[80:81], v[224:225], v[166:167] op_sel_hi:[1,0,1]
	s_nop 0
	v_pk_fma_f32 v[162:163], v[82:83], v[224:225], v[166:167] op_sel:[0,1,0]
	s_nop 0
	v_pk_fma_f32 v[162:163], v[86:87], v[226:227], v[162:163] op_sel_hi:[1,0,1]
	v_mov_b32_e32 v164, v227
	v_pk_fma_f32 v[166:167], v[90:91], v[164:165], v[162:163] op_sel_hi:[1,0,1]
	ds_read_b128 v[240:243], v182 offset:50176
	s_waitcnt lgkmcnt(3)
	v_pk_fma_f32 v[166:167], v[76:77], v[228:229], v[166:167] op_sel_hi:[1,0,1]
	s_nop 0
	v_pk_fma_f32 v[162:163], v[78:79], v[228:229], v[166:167] op_sel:[0,1,0]
	s_nop 0
	v_pk_fma_f32 v[162:163], v[84:85], v[230:231], v[162:163] op_sel_hi:[1,0,1]
	v_mov_b32_e32 v164, v231
	v_pk_fma_f32 v[166:167], v[88:89], v[164:165], v[162:163] op_sel_hi:[1,0,1]
	ds_read_b128 v[224:227], v182 offset:51200
	s_waitcnt lgkmcnt(3)
	v_pk_fma_f32 v[166:167], v[68:69], v[232:233], v[166:167] op_sel_hi:[1,0,1]
	s_nop 0
	v_pk_fma_f32 v[162:163], v[70:71], v[232:233], v[166:167] op_sel:[0,1,0]
	s_nop 0
	v_pk_fma_f32 v[162:163], v[72:73], v[234:235], v[162:163] op_sel_hi:[1,0,1]
	v_mov_b32_e32 v164, v235
	v_pk_fma_f32 v[162:163], v[74:75], v[164:165], v[162:163] op_sel_hi:[1,0,1]
	ds_read_b128 v[228:231], v182 offset:52224
	s_waitcnt lgkmcnt(3)
	v_pk_fma_f32 v[168:169], v[124:125], v[236:237], 0 op_sel_hi:[1,0,0]
	s_nop 0
	v_pk_fma_f32 v[164:165], v[126:127], v[236:237], v[168:169] op_sel:[0,1,0]
	s_nop 0
	v_pk_fma_f32 v[164:165], v[128:129], v[238:239], v[164:165] op_sel_hi:[1,0,1]
	v_mov_b32_e32 v166, v239
	v_pk_fma_f32 v[168:169], v[130:131], v[166:167], v[164:165] op_sel_hi:[1,0,1]
	ds_read_b128 v[232:235], v182 offset:53248
	s_waitcnt lgkmcnt(3)
	v_pk_fma_f32 v[168:169], v[112:113], v[240:241], v[168:169] op_sel_hi:[1,0,1]
	s_nop 0
	v_pk_fma_f32 v[164:165], v[114:115], v[240:241], v[168:169] op_sel:[0,1,0]
	s_nop 0
	v_pk_fma_f32 v[164:165], v[118:119], v[242:243], v[164:165] op_sel_hi:[1,0,1]
	v_mov_b32_e32 v166, v243
	v_pk_fma_f32 v[168:169], v[122:123], v[166:167], v[164:165] op_sel_hi:[1,0,1]
	ds_read_b128 v[236:239], v182 offset:54272
	s_waitcnt lgkmcnt(3)
	v_pk_fma_f32 v[168:169], v[108:109], v[224:225], v[168:169] op_sel_hi:[1,0,1]
	s_nop 0
	v_pk_fma_f32 v[164:165], v[110:111], v[224:225], v[168:169] op_sel:[0,1,0]
	s_nop 0
	v_pk_fma_f32 v[164:165], v[116:117], v[226:227], v[164:165] op_sel_hi:[1,0,1]
	v_mov_b32_e32 v166, v227
	v_pk_fma_f32 v[168:169], v[120:121], v[166:167], v[164:165] op_sel_hi:[1,0,1]
	ds_read_b128 v[240:243], v182 offset:55296
	s_waitcnt lgkmcnt(3)
	v_pk_fma_f32 v[168:169], v[96:97], v[228:229], v[168:169] op_sel_hi:[1,0,1]
	s_nop 0
	v_pk_fma_f32 v[164:165], v[98:99], v[228:229], v[168:169] op_sel:[0,1,0]
	s_nop 0
	v_pk_fma_f32 v[164:165], v[102:103], v[230:231], v[164:165] op_sel_hi:[1,0,1]
	v_mov_b32_e32 v166, v231
	v_pk_fma_f32 v[168:169], v[106:107], v[166:167], v[164:165] op_sel_hi:[1,0,1]
	ds_read_b128 v[224:227], v182 offset:56320
	s_waitcnt lgkmcnt(3)
	v_pk_fma_f32 v[168:169], v[92:93], v[232:233], v[168:169] op_sel_hi:[1,0,1]
	s_nop 0
	v_pk_fma_f32 v[164:165], v[94:95], v[232:233], v[168:169] op_sel:[0,1,0]
	s_nop 0
	v_pk_fma_f32 v[164:165], v[100:101], v[234:235], v[164:165] op_sel_hi:[1,0,1]
	v_mov_b32_e32 v166, v235
	v_pk_fma_f32 v[168:169], v[104:105], v[166:167], v[164:165] op_sel_hi:[1,0,1]
	ds_read_b128 v[228:231], v182 offset:57344
	s_waitcnt lgkmcnt(3)
	v_pk_fma_f32 v[168:169], v[80:81], v[236:237], v[168:169] op_sel_hi:[1,0,1]
	s_nop 0
	v_pk_fma_f32 v[164:165], v[82:83], v[236:237], v[168:169] op_sel:[0,1,0]
	s_nop 0
	v_pk_fma_f32 v[164:165], v[86:87], v[238:239], v[164:165] op_sel_hi:[1,0,1]
	v_mov_b32_e32 v166, v239
	v_pk_fma_f32 v[168:169], v[90:91], v[166:167], v[164:165] op_sel_hi:[1,0,1]
	ds_read_b128 v[232:235], v182 offset:58368
	s_waitcnt lgkmcnt(3)
; #define LAS __attribute__((address_space(3)))
; __device__ __forceinline__ void phase_norm2(const Params& p, const Ctx& F, const int l) {
;     ...
; #pragma unroll
;         for (int e = 0; e < 16; ++e) { f32x2 a = {0.f, 0.f};
; #pragma unroll
;             for (int j = 0; j < 8; ++j) { const f32x4 w = *((const LAS f32x4*)(wr2 + e * DM) + F.lane + 64 * j);
; #pragma unroll
;                 for (int c = 0; c < 4; ++c) a += vv[j][c] * w[c]; }
;             lg[e] = a; }
	v_pk_fma_f32 v[168:169], v[76:77], v[240:241], v[168:169] op_sel_hi:[1,0,1]
	s_nop 0
	v_pk_fma_f32 v[164:165], v[78:79], v[240:241], v[168:169] op_sel:[0,1,0]
	s_nop 0
	v_pk_fma_f32 v[164:165], v[84:85], v[242:243], v[164:165] op_sel_hi:[1,0,1]
	v_mov_b32_e32 v166, v243
	v_pk_fma_f32 v[168:169], v[88:89], v[166:167], v[164:165] op_sel_hi:[1,0,1]
	ds_read_b128 v[236:239], v182 offset:59392
	s_waitcnt lgkmcnt(3)
	v_pk_fma_f32 v[168:169], v[68:69], v[224:225], v[168:169] op_sel_hi:[1,0,1]
	s_nop 0
	v_pk_fma_f32 v[164:165], v[70:71], v[224:225], v[168:169] op_sel:[0,1,0]
	s_nop 0
	v_pk_fma_f32 v[164:165], v[72:73], v[226:227], v[164:165] op_sel_hi:[1,0,1]
	v_mov_b32_e32 v166, v227
	v_pk_fma_f32 v[164:165], v[74:75], v[166:167], v[164:165] op_sel_hi:[1,0,1]
	ds_read_b128 v[240:243], v182 offset:60416
	s_waitcnt lgkmcnt(3)
	v_pk_fma_f32 v[170:171], v[124:125], v[228:229], 0 op_sel_hi:[1,0,0]
	s_nop 0
	v_pk_fma_f32 v[166:167], v[126:127], v[228:229], v[170:171] op_sel:[0,1,0]
	s_nop 0
	v_pk_fma_f32 v[166:167], v[128:129], v[230:231], v[166:167] op_sel_hi:[1,0,1]
	v_mov_b32_e32 v168, v231
	v_pk_fma_f32 v[170:171], v[130:131], v[168:169], v[166:167] op_sel_hi:[1,0,1]
	ds_read_b128 v[224:227], v182 offset:61440
	s_waitcnt lgkmcnt(3)
	v_pk_fma_f32 v[170:171], v[112:113], v[232:233], v[170:171] op_sel_hi:[1,0,1]
	s_nop 0
	v_pk_fma_f32 v[166:167], v[114:115], v[232:233], v[170:171] op_sel:[0,1,0]
	s_nop 0
	v_pk_fma_f32 v[166:167], v[118:119], v[234:235], v[166:167] op_sel_hi:[1,0,1]
	v_mov_b32_e32 v168, v235
	v_pk_fma_f32 v[170:171], v[122:123], v[168:169], v[166:167] op_sel_hi:[1,0,1]
	ds_read_b128 v[228:231], v182 offset:62464
	s_waitcnt lgkmcnt(3)
	v_pk_fma_f32 v[170:171], v[108:109], v[236:237], v[170:171] op_sel_hi:[1,0,1]
	s_nop 0
	v_pk_fma_f32 v[166:167], v[110:111], v[236:237], v[170:171] op_sel:[0,1,0]
	s_nop 0
	v_pk_fma_f32 v[166:167], v[116:117], v[238:239], v[166:167] op_sel_hi:[1,0,1]
	v_mov_b32_e32 v168, v239
	v_pk_fma_f32 v[170:171], v[120:121], v[168:169], v[166:167] op_sel_hi:[1,0,1]
	ds_read_b128 v[232:235], v182 offset:63488
	s_waitcnt lgkmcnt(3)
	v_pk_fma_f32 v[170:171], v[96:97], v[240:241], v[170:171] op_sel_hi:[1,0,1]
	s_nop 0
	v_pk_fma_f32 v[166:167], v[98:99], v[240:241], v[170:171] op_sel:[0,1,0]
	s_nop 0
	v_pk_fma_f32 v[166:167], v[102:103], v[242:243], v[166:167] op_sel_hi:[1,0,1]
	v_mov_b32_e32 v168, v243
	v_pk_fma_f32 v[170:171], v[106:107], v[168:169], v[166:167] op_sel_hi:[1,0,1]
	ds_read_b128 v[236:239], v182 offset:64512
	s_waitcnt lgkmcnt(3)
	v_pk_fma_f32 v[170:171], v[92:93], v[224:225], v[170:171] op_sel_hi:[1,0,1]
	s_nop 0
	v_pk_fma_f32 v[166:167], v[94:95], v[224:225], v[170:171] op_sel:[0,1,0]
	s_nop 0
	v_pk_fma_f32 v[166:167], v[100:101], v[226:227], v[166:167] op_sel_hi:[1,0,1]
	v_mov_b32_e32 v168, v227
	v_pk_fma_f32 v[170:171], v[104:105], v[168:169], v[166:167] op_sel_hi:[1,0,1]
	ds_read_b128 v[240:243], v244
	s_waitcnt lgkmcnt(3)
	v_pk_fma_f32 v[170:171], v[80:81], v[228:229], v[170:171] op_sel_hi:[1,0,1]
	s_nop 0
	v_pk_fma_f32 v[166:167], v[82:83], v[228:229], v[170:171] op_sel:[0,1,0]
	s_nop 0
	v_pk_fma_f32 v[166:167], v[86:87], v[230:231], v[166:167] op_sel_hi:[1,0,1]
	v_mov_b32_e32 v168, v231
	v_pk_fma_f32 v[170:171], v[90:91], v[168:169], v[166:167] op_sel_hi:[1,0,1]
	ds_read_b128 v[224:227], v244 offset:1024
	s_waitcnt lgkmcnt(3)
	v_pk_fma_f32 v[170:171], v[76:77], v[232:233], v[170:171] op_sel_hi:[1,0,1]
	s_nop 0
	v_pk_fma_f32 v[166:167], v[78:79], v[232:233], v[170:171] op_sel:[0,1,0]
	s_nop 0
	v_pk_fma_f32 v[166:167], v[84:85], v[234:235], v[166:167] op_sel_hi:[1,0,1]
	v_mov_b32_e32 v168, v235
	v_pk_fma_f32 v[170:171], v[88:89], v[168:169], v[166:167] op_sel_hi:[1,0,1]
	ds_read_b128 v[228:231], v244 offset:2048
	s_waitcnt lgkmcnt(3)
	v_pk_fma_f32 v[170:171], v[68:69], v[236:237], v[170:171] op_sel_hi:[1,0,1]
	s_nop 0
	v_pk_fma_f32 v[166:167], v[70:71], v[236:237], v[170:171] op_sel:[0,1,0]
	s_nop 0
	v_pk_fma_f32 v[166:167], v[72:73], v[238:239], v[166:167] op_sel_hi:[1,0,1]
	v_mov_b32_e32 v168, v239
	v_pk_fma_f32 v[166:167], v[74:75], v[168:169], v[166:167] op_sel_hi:[1,0,1]
	ds_read_b128 v[232:235], v244 offset:3072
	s_waitcnt lgkmcnt(3)
	v_pk_fma_f32 v[172:173], v[124:125], v[240:241], 0 op_sel_hi:[1,0,0]
	s_nop 0
	v_pk_fma_f32 v[168:169], v[126:127], v[240:241], v[172:173] op_sel:[0,1,0]
	s_nop 0
	v_pk_fma_f32 v[168:169], v[128:129], v[242:243], v[168:169] op_sel_hi:[1,0,1]
	v_mov_b32_e32 v170, v243
	v_pk_fma_f32 v[172:173], v[130:131], v[170:171], v[168:169] op_sel_hi:[1,0,1]
	ds_read_b128 v[236:239], v244 offset:4096
	s_waitcnt lgkmcnt(3)
	v_pk_fma_f32 v[172:173], v[112:113], v[224:225], v[172:173] op_sel_hi:[1,0,1]
	s_nop 0
	v_pk_fma_f32 v[168:169], v[114:115], v[224:225], v[172:173] op_sel:[0,1,0]
	s_nop 0
	v_pk_fma_f32 v[168:169], v[118:119], v[226:227], v[168:169] op_sel_hi:[1,0,1]
	v_mov_b32_e32 v170, v227
	v_pk_fma_f32 v[172:173], v[122:123], v[170:171], v[168:169] op_sel_hi:[1,0,1]
	ds_read_b128 v[240:243], v244 offset:5120
	s_waitcnt lgkmcnt(3)
	v_pk_fma_f32 v[172:173], v[108:109], v[228:229], v[172:173] op_sel_hi:[1,0,1]
	s_nop 0
	v_pk_fma_f32 v[168:169], v[110:111], v[228:229], v[172:173] op_sel:[0,1,0]
	s_nop 0
	v_pk_fma_f32 v[168:169], v[116:117], v[230:231], v[168:169] op_sel_hi:[1,0,1]
	v_mov_b32_e32 v170, v231
	v_pk_fma_f32 v[172:173], v[120:121], v[170:171], v[168:169] op_sel_hi:[1,0,1]
	ds_read_b128 v[224:227], v244 offset:6144
	s_waitcnt lgkmcnt(3)
	v_pk_fma_f32 v[172:173], v[96:97], v[232:233], v[172:173] op_sel_hi:[1,0,1]
	s_nop 0
	v_pk_fma_f32 v[168:169], v[98:99], v[232:233], v[172:173] op_sel:[0,1,0]
	s_nop 0
	v_pk_fma_f32 v[168:169], v[102:103], v[234:235], v[168:169] op_sel_hi:[1,0,1]
	v_mov_b32_e32 v170, v235
	v_pk_fma_f32 v[172:173], v[106:107], v[170:171], v[168:169] op_sel_hi:[1,0,1]
	ds_read_b128 v[228:231], v244 offset:7168
	s_waitcnt lgkmcnt(3)
; #define LAS __attribute__((address_space(3)))
; __device__ __forceinline__ void phase_norm2(const Params& p, const Ctx& F, const int l) {
;     ...
; #pragma unroll
;         for (int e = 0; e < 16; ++e) { f32x2 a = {0.f, 0.f};
; #pragma unroll
;             for (int j = 0; j < 8; ++j) { const f32x4 w = *((const LAS f32x4*)(wr2 + e * DM) + F.lane + 64 * j);
; #pragma unroll
;                 for (int c = 0; c < 4; ++c) a += vv[j][c] * w[c]; }
;             lg[e] = a; }
	v_pk_fma_f32 v[172:173], v[92:93], v[236:237], v[172:173] op_sel_hi:[1,0,1]
	s_nop 0
	v_pk_fma_f32 v[168:169], v[94:95], v[236:237], v[172:173] op_sel:[0,1,0]
	s_nop 0
	v_pk_fma_f32 v[168:169], v[100:101], v[238:239], v[168:169] op_sel_hi:[1,0,1]
	v_mov_b32_e32 v170, v239
	v_pk_fma_f32 v[172:173], v[104:105], v[170:171], v[168:169] op_sel_hi:[1,0,1]
	ds_read_b128 v[232:235], v244 offset:8192
	s_waitcnt lgkmcnt(3)
	v_pk_fma_f32 v[172:173], v[80:81], v[240:241], v[172:173] op_sel_hi:[1,0,1]
	s_nop 0
	v_pk_fma_f32 v[168:169], v[82:83], v[240:241], v[172:173] op_sel:[0,1,0]
	s_nop 0
	v_pk_fma_f32 v[168:169], v[86:87], v[242:243], v[168:169] op_sel_hi:[1,0,1]
	v_mov_b32_e32 v170, v243
	v_pk_fma_f32 v[172:173], v[90:91], v[170:171], v[168:169] op_sel_hi:[1,0,1]
	ds_read_b128 v[236:239], v244 offset:9216
	s_waitcnt lgkmcnt(3)
	v_pk_fma_f32 v[172:173], v[76:77], v[224:225], v[172:173] op_sel_hi:[1,0,1]
	s_nop 0
	v_pk_fma_f32 v[168:169], v[78:79], v[224:225], v[172:173] op_sel:[0,1,0]
	s_nop 0
	v_pk_fma_f32 v[168:169], v[84:85], v[226:227], v[168:169] op_sel_hi:[1,0,1]
	v_mov_b32_e32 v170, v227
	v_pk_fma_f32 v[172:173], v[88:89], v[170:171], v[168:169] op_sel_hi:[1,0,1]
	ds_read_b128 v[240:243], v244 offset:10240
	s_waitcnt lgkmcnt(3)
	v_pk_fma_f32 v[172:173], v[68:69], v[228:229], v[172:173] op_sel_hi:[1,0,1]
	s_nop 0
	v_pk_fma_f32 v[168:169], v[70:71], v[228:229], v[172:173] op_sel:[0,1,0]
	s_nop 0
	v_pk_fma_f32 v[168:169], v[72:73], v[230:231], v[168:169] op_sel_hi:[1,0,1]
	v_mov_b32_e32 v170, v231
	v_pk_fma_f32 v[168:169], v[74:75], v[170:171], v[168:169] op_sel_hi:[1,0,1]
	ds_read_b128 v[224:227], v244 offset:11264
	s_waitcnt lgkmcnt(3)
	v_pk_fma_f32 v[174:175], v[124:125], v[232:233], 0 op_sel_hi:[1,0,0]
	s_nop 0
	v_pk_fma_f32 v[170:171], v[126:127], v[232:233], v[174:175] op_sel:[0,1,0]
	s_nop 0
	v_pk_fma_f32 v[170:171], v[128:129], v[234:235], v[170:171] op_sel_hi:[1,0,1]
	v_mov_b32_e32 v172, v235
	v_pk_fma_f32 v[174:175], v[130:131], v[172:173], v[170:171] op_sel_hi:[1,0,1]
	ds_read_b128 v[228:231], v244 offset:12288
	s_waitcnt lgkmcnt(3)
	v_pk_fma_f32 v[174:175], v[112:113], v[236:237], v[174:175] op_sel_hi:[1,0,1]
	s_nop 0
	v_pk_fma_f32 v[170:171], v[114:115], v[236:237], v[174:175] op_sel:[0,1,0]
	s_nop 0
	v_pk_fma_f32 v[170:171], v[118:119], v[238:239], v[170:171] op_sel_hi:[1,0,1]
	v_mov_b32_e32 v172, v239
	v_pk_fma_f32 v[174:175], v[122:123], v[172:173], v[170:171] op_sel_hi:[1,0,1]
	ds_read_b128 v[232:235], v244 offset:13312
	s_waitcnt lgkmcnt(3)
	v_pk_fma_f32 v[174:175], v[108:109], v[240:241], v[174:175] op_sel_hi:[1,0,1]
	s_nop 0
	v_pk_fma_f32 v[170:171], v[110:111], v[240:241], v[174:175] op_sel:[0,1,0]
	s_nop 0
	v_pk_fma_f32 v[170:171], v[116:117], v[242:243], v[170:171] op_sel_hi:[1,0,1]
	v_mov_b32_e32 v172, v243
	v_pk_fma_f32 v[174:175], v[120:121], v[172:173], v[170:171] op_sel_hi:[1,0,1]
	ds_read_b128 v[236:239], v244 offset:14336
	s_waitcnt lgkmcnt(3)
	v_pk_fma_f32 v[174:175], v[96:97], v[224:225], v[174:175] op_sel_hi:[1,0,1]
	s_nop 0
	v_pk_fma_f32 v[170:171], v[98:99], v[224:225], v[174:175] op_sel:[0,1,0]
	s_nop 0
	v_pk_fma_f32 v[170:171], v[102:103], v[226:227], v[170:171] op_sel_hi:[1,0,1]
	v_mov_b32_e32 v172, v227
	v_pk_fma_f32 v[174:175], v[106:107], v[172:173], v[170:171] op_sel_hi:[1,0,1]
	ds_read_b128 v[240:243], v244 offset:15360
	s_waitcnt lgkmcnt(3)
	v_pk_fma_f32 v[174:175], v[92:93], v[228:229], v[174:175] op_sel_hi:[1,0,1]
	s_nop 0
	v_pk_fma_f32 v[170:171], v[94:95], v[228:229], v[174:175] op_sel:[0,1,0]
	s_nop 0
	v_pk_fma_f32 v[170:171], v[100:101], v[230:231], v[170:171] op_sel_hi:[1,0,1]
	v_mov_b32_e32 v172, v231
	v_pk_fma_f32 v[174:175], v[104:105], v[172:173], v[170:171] op_sel_hi:[1,0,1]
	ds_read_b128 v[224:227], v244 offset:16384
	s_waitcnt lgkmcnt(3)
	v_pk_fma_f32 v[174:175], v[80:81], v[232:233], v[174:175] op_sel_hi:[1,0,1]
	s_nop 0
	v_pk_fma_f32 v[170:171], v[82:83], v[232:233], v[174:175] op_sel:[0,1,0]
	s_nop 0
	v_pk_fma_f32 v[170:171], v[86:87], v[234:235], v[170:171] op_sel_hi:[1,0,1]
	v_mov_b32_e32 v172, v235
	v_pk_fma_f32 v[174:175], v[90:91], v[172:173], v[170:171] op_sel_hi:[1,0,1]
	ds_read_b128 v[228:231], v244 offset:17408
	s_waitcnt lgkmcnt(3)
	v_pk_fma_f32 v[174:175], v[76:77], v[236:237], v[174:175] op_sel_hi:[1,0,1]
	s_nop 0
	v_pk_fma_f32 v[170:171], v[78:79], v[236:237], v[174:175] op_sel:[0,1,0]
	s_nop 0
	v_pk_fma_f32 v[170:171], v[84:85], v[238:239], v[170:171] op_sel_hi:[1,0,1]
	v_mov_b32_e32 v172, v239
	v_pk_fma_f32 v[174:175], v[88:89], v[172:173], v[170:171] op_sel_hi:[1,0,1]
	ds_read_b128 v[232:235], v244 offset:18432
	s_waitcnt lgkmcnt(3)
	v_pk_fma_f32 v[174:175], v[68:69], v[240:241], v[174:175] op_sel_hi:[1,0,1]
	s_nop 0
	v_pk_fma_f32 v[170:171], v[70:71], v[240:241], v[174:175] op_sel:[0,1,0]
	s_nop 0
	v_pk_fma_f32 v[170:171], v[72:73], v[242:243], v[170:171] op_sel_hi:[1,0,1]
	v_mov_b32_e32 v172, v243
	v_pk_fma_f32 v[170:171], v[74:75], v[172:173], v[170:171] op_sel_hi:[1,0,1]
	ds_read_b128 v[236:239], v244 offset:19456
	s_waitcnt lgkmcnt(3)
	v_pk_fma_f32 v[176:177], v[124:125], v[224:225], 0 op_sel_hi:[1,0,0]
	s_nop 0
	v_pk_fma_f32 v[172:173], v[126:127], v[224:225], v[176:177] op_sel:[0,1,0]
	s_nop 0
	v_pk_fma_f32 v[172:173], v[128:129], v[226:227], v[172:173] op_sel_hi:[1,0,1]
	v_mov_b32_e32 v174, v227
	v_pk_fma_f32 v[176:177], v[130:131], v[174:175], v[172:173] op_sel_hi:[1,0,1]
	ds_read_b128 v[240:243], v244 offset:20480
	s_waitcnt lgkmcnt(3)
	v_pk_fma_f32 v[176:177], v[112:113], v[228:229], v[176:177] op_sel_hi:[1,0,1]
	s_nop 0
	v_pk_fma_f32 v[172:173], v[114:115], v[228:229], v[176:177] op_sel:[0,1,0]
	s_nop 0
	v_pk_fma_f32 v[172:173], v[118:119], v[230:231], v[172:173] op_sel_hi:[1,0,1]
	v_mov_b32_e32 v174, v231
	v_pk_fma_f32 v[176:177], v[122:123], v[174:175], v[172:173] op_sel_hi:[1,0,1]
	ds_read_b128 v[224:227], v244 offset:21504
	s_waitcnt lgkmcnt(3)
; #define LAS __attribute__((address_space(3)))
; __device__ __forceinline__ void phase_norm2(const Params& p, const Ctx& F, const int l) {
;     ...
; #pragma unroll
;         for (int e = 0; e < 16; ++e) { f32x2 a = {0.f, 0.f};
; #pragma unroll
;             for (int j = 0; j < 8; ++j) { const f32x4 w = *((const LAS f32x4*)(wr2 + e * DM) + F.lane + 64 * j);
; #pragma unroll
;                 for (int c = 0; c < 4; ++c) a += vv[j][c] * w[c]; }
;             lg[e] = a; }
	v_pk_fma_f32 v[176:177], v[108:109], v[232:233], v[176:177] op_sel_hi:[1,0,1]
	s_nop 0
	v_pk_fma_f32 v[172:173], v[110:111], v[232:233], v[176:177] op_sel:[0,1,0]
	s_nop 0
	v_pk_fma_f32 v[172:173], v[116:117], v[234:235], v[172:173] op_sel_hi:[1,0,1]
	v_mov_b32_e32 v174, v235
	v_pk_fma_f32 v[176:177], v[120:121], v[174:175], v[172:173] op_sel_hi:[1,0,1]
	ds_read_b128 v[228:231], v244 offset:22528
	s_waitcnt lgkmcnt(3)
	v_pk_fma_f32 v[176:177], v[96:97], v[236:237], v[176:177] op_sel_hi:[1,0,1]
	s_nop 0
	v_pk_fma_f32 v[172:173], v[98:99], v[236:237], v[176:177] op_sel:[0,1,0]
	s_nop 0
	v_pk_fma_f32 v[172:173], v[102:103], v[238:239], v[172:173] op_sel_hi:[1,0,1]
	v_mov_b32_e32 v174, v239
	v_pk_fma_f32 v[176:177], v[106:107], v[174:175], v[172:173] op_sel_hi:[1,0,1]
	ds_read_b128 v[232:235], v244 offset:23552
	s_waitcnt lgkmcnt(3)
	v_pk_fma_f32 v[176:177], v[92:93], v[240:241], v[176:177] op_sel_hi:[1,0,1]
	s_nop 0
	v_pk_fma_f32 v[172:173], v[94:95], v[240:241], v[176:177] op_sel:[0,1,0]
	s_nop 0
	v_pk_fma_f32 v[172:173], v[100:101], v[242:243], v[172:173] op_sel_hi:[1,0,1]
	v_mov_b32_e32 v174, v243
	v_pk_fma_f32 v[176:177], v[104:105], v[174:175], v[172:173] op_sel_hi:[1,0,1]
	ds_read_b128 v[236:239], v244 offset:24576
	s_waitcnt lgkmcnt(3)
	v_pk_fma_f32 v[176:177], v[80:81], v[224:225], v[176:177] op_sel_hi:[1,0,1]
	s_nop 0
	v_pk_fma_f32 v[172:173], v[82:83], v[224:225], v[176:177] op_sel:[0,1,0]
	s_nop 0
	v_pk_fma_f32 v[172:173], v[86:87], v[226:227], v[172:173] op_sel_hi:[1,0,1]
	v_mov_b32_e32 v174, v227
	v_pk_fma_f32 v[176:177], v[90:91], v[174:175], v[172:173] op_sel_hi:[1,0,1]
	ds_read_b128 v[240:243], v244 offset:25600
	s_waitcnt lgkmcnt(3)
	v_pk_fma_f32 v[176:177], v[76:77], v[228:229], v[176:177] op_sel_hi:[1,0,1]
	s_nop 0
	v_pk_fma_f32 v[172:173], v[78:79], v[228:229], v[176:177] op_sel:[0,1,0]
	s_nop 0
	v_pk_fma_f32 v[172:173], v[84:85], v[230:231], v[172:173] op_sel_hi:[1,0,1]
	v_mov_b32_e32 v174, v231
	v_pk_fma_f32 v[176:177], v[88:89], v[174:175], v[172:173] op_sel_hi:[1,0,1]
	ds_read_b128 v[224:227], v244 offset:26624
	s_waitcnt lgkmcnt(3)
	v_pk_fma_f32 v[176:177], v[68:69], v[232:233], v[176:177] op_sel_hi:[1,0,1]
	s_nop 0
	v_pk_fma_f32 v[172:173], v[70:71], v[232:233], v[176:177] op_sel:[0,1,0]
	s_nop 0
	v_pk_fma_f32 v[172:173], v[72:73], v[234:235], v[172:173] op_sel_hi:[1,0,1]
	v_mov_b32_e32 v174, v235
	v_pk_fma_f32 v[172:173], v[74:75], v[174:175], v[172:173] op_sel_hi:[1,0,1]
	ds_read_b128 v[228:231], v244 offset:27648
	s_waitcnt lgkmcnt(3)
	v_pk_fma_f32 v[178:179], v[124:125], v[236:237], 0 op_sel_hi:[1,0,0]
	s_nop 0
	v_pk_fma_f32 v[174:175], v[126:127], v[236:237], v[178:179] op_sel:[0,1,0]
	s_nop 0
	v_pk_fma_f32 v[174:175], v[128:129], v[238:239], v[174:175] op_sel_hi:[1,0,1]
	v_mov_b32_e32 v176, v239
	v_pk_fma_f32 v[178:179], v[130:131], v[176:177], v[174:175] op_sel_hi:[1,0,1]
	ds_read_b128 v[232:235], v244 offset:28672
	s_waitcnt lgkmcnt(3)
	v_pk_fma_f32 v[178:179], v[112:113], v[240:241], v[178:179] op_sel_hi:[1,0,1]
	s_nop 0
	v_pk_fma_f32 v[174:175], v[114:115], v[240:241], v[178:179] op_sel:[0,1,0]
	s_nop 0
	v_pk_fma_f32 v[174:175], v[118:119], v[242:243], v[174:175] op_sel_hi:[1,0,1]
	v_mov_b32_e32 v176, v243
	v_pk_fma_f32 v[178:179], v[122:123], v[176:177], v[174:175] op_sel_hi:[1,0,1]
	ds_read_b128 v[236:239], v244 offset:29696
	s_waitcnt lgkmcnt(3)
	v_pk_fma_f32 v[178:179], v[108:109], v[224:225], v[178:179] op_sel_hi:[1,0,1]
	s_nop 0
	v_pk_fma_f32 v[174:175], v[110:111], v[224:225], v[178:179] op_sel:[0,1,0]
	s_nop 0
	v_pk_fma_f32 v[174:175], v[116:117], v[226:227], v[174:175] op_sel_hi:[1,0,1]
	v_mov_b32_e32 v176, v227
	v_pk_fma_f32 v[178:179], v[120:121], v[176:177], v[174:175] op_sel_hi:[1,0,1]
	ds_read_b128 v[240:243], v244 offset:30720
	s_waitcnt lgkmcnt(3)
	v_pk_fma_f32 v[178:179], v[96:97], v[228:229], v[178:179] op_sel_hi:[1,0,1]
	s_nop 0
	v_pk_fma_f32 v[174:175], v[98:99], v[228:229], v[178:179] op_sel:[0,1,0]
	s_nop 0
	v_pk_fma_f32 v[174:175], v[102:103], v[230:231], v[174:175] op_sel_hi:[1,0,1]
	v_mov_b32_e32 v176, v231
	v_pk_fma_f32 v[178:179], v[106:107], v[176:177], v[174:175] op_sel_hi:[1,0,1]
	ds_read_b128 v[224:227], v244 offset:31744
	s_waitcnt lgkmcnt(3)
	v_pk_fma_f32 v[178:179], v[92:93], v[232:233], v[178:179] op_sel_hi:[1,0,1]
	s_nop 0
	v_pk_fma_f32 v[174:175], v[94:95], v[232:233], v[178:179] op_sel:[0,1,0]
	s_nop 0
	v_pk_fma_f32 v[174:175], v[100:101], v[234:235], v[174:175] op_sel_hi:[1,0,1]
	v_mov_b32_e32 v176, v235
	v_pk_fma_f32 v[178:179], v[104:105], v[176:177], v[174:175] op_sel_hi:[1,0,1]
	ds_read_b128 v[228:231], v244 offset:32768
	s_waitcnt lgkmcnt(3)
	v_pk_fma_f32 v[178:179], v[80:81], v[236:237], v[178:179] op_sel_hi:[1,0,1]
	s_nop 0
	v_pk_fma_f32 v[174:175], v[82:83], v[236:237], v[178:179] op_sel:[0,1,0]
	s_nop 0
	v_pk_fma_f32 v[174:175], v[86:87], v[238:239], v[174:175] op_sel_hi:[1,0,1]
	v_mov_b32_e32 v176, v239
	v_pk_fma_f32 v[178:179], v[90:91], v[176:177], v[174:175] op_sel_hi:[1,0,1]
	ds_read_b128 v[232:235], v244 offset:33792
	s_waitcnt lgkmcnt(3)
	v_pk_fma_f32 v[178:179], v[76:77], v[240:241], v[178:179] op_sel_hi:[1,0,1]
	s_nop 0
	v_pk_fma_f32 v[174:175], v[78:79], v[240:241], v[178:179] op_sel:[0,1,0]
	s_nop 0
	v_pk_fma_f32 v[174:175], v[84:85], v[242:243], v[174:175] op_sel_hi:[1,0,1]
	v_mov_b32_e32 v176, v243
	v_pk_fma_f32 v[178:179], v[88:89], v[176:177], v[174:175] op_sel_hi:[1,0,1]
	ds_read_b128 v[236:239], v244 offset:34816
	s_waitcnt lgkmcnt(3)
; #define LAS __attribute__((address_space(3)))
; __device__ __forceinline__ void phase_norm2(const Params& p, const Ctx& F, const int l) {
;     ...
; #pragma unroll
;         for (int e = 0; e < 16; ++e) { f32x2 a = {0.f, 0.f};
; #pragma unroll
;             for (int j = 0; j < 8; ++j) { const f32x4 w = *((const LAS f32x4*)(wr2 + e * DM) + F.lane + 64 * j);
; #pragma unroll
;                 for (int c = 0; c < 4; ++c) a += vv[j][c] * w[c]; }
;             lg[e] = a; }
	v_pk_fma_f32 v[178:179], v[68:69], v[224:225], v[178:179] op_sel_hi:[1,0,1]
	s_nop 0
	v_pk_fma_f32 v[174:175], v[70:71], v[224:225], v[178:179] op_sel:[0,1,0]
	s_nop 0
	v_pk_fma_f32 v[174:175], v[72:73], v[226:227], v[174:175] op_sel_hi:[1,0,1]
	v_mov_b32_e32 v176, v227
	v_pk_fma_f32 v[174:175], v[74:75], v[176:177], v[174:175] op_sel_hi:[1,0,1]
	ds_read_b128 v[240:243], v244 offset:35840
	s_waitcnt lgkmcnt(3)
	v_pk_fma_f32 v[180:181], v[124:125], v[228:229], 0 op_sel_hi:[1,0,0]
	s_nop 0
	v_pk_fma_f32 v[176:177], v[126:127], v[228:229], v[180:181] op_sel:[0,1,0]
	s_nop 0
	v_pk_fma_f32 v[176:177], v[128:129], v[230:231], v[176:177] op_sel_hi:[1,0,1]
	v_mov_b32_e32 v178, v231
	v_pk_fma_f32 v[180:181], v[130:131], v[178:179], v[176:177] op_sel_hi:[1,0,1]
	ds_read_b128 v[224:227], v244 offset:36864
	s_waitcnt lgkmcnt(3)
	v_pk_fma_f32 v[180:181], v[112:113], v[232:233], v[180:181] op_sel_hi:[1,0,1]
	s_nop 0
	v_pk_fma_f32 v[176:177], v[114:115], v[232:233], v[180:181] op_sel:[0,1,0]
	s_nop 0
	v_pk_fma_f32 v[176:177], v[118:119], v[234:235], v[176:177] op_sel_hi:[1,0,1]
	v_mov_b32_e32 v178, v235
	v_pk_fma_f32 v[180:181], v[122:123], v[178:179], v[176:177] op_sel_hi:[1,0,1]
	ds_read_b128 v[228:231], v244 offset:37888
	s_waitcnt lgkmcnt(3)
	v_pk_fma_f32 v[180:181], v[108:109], v[236:237], v[180:181] op_sel_hi:[1,0,1]
	s_nop 0
	v_pk_fma_f32 v[176:177], v[110:111], v[236:237], v[180:181] op_sel:[0,1,0]
	s_nop 0
	v_pk_fma_f32 v[176:177], v[116:117], v[238:239], v[176:177] op_sel_hi:[1,0,1]
	v_mov_b32_e32 v178, v239
	v_pk_fma_f32 v[180:181], v[120:121], v[178:179], v[176:177] op_sel_hi:[1,0,1]
	ds_read_b128 v[232:235], v244 offset:38912
	s_waitcnt lgkmcnt(3)
	v_pk_fma_f32 v[180:181], v[96:97], v[240:241], v[180:181] op_sel_hi:[1,0,1]
	s_nop 0
	v_pk_fma_f32 v[176:177], v[98:99], v[240:241], v[180:181] op_sel:[0,1,0]
	s_nop 0
	v_pk_fma_f32 v[176:177], v[102:103], v[242:243], v[176:177] op_sel_hi:[1,0,1]
	v_mov_b32_e32 v178, v243
	v_pk_fma_f32 v[180:181], v[106:107], v[178:179], v[176:177] op_sel_hi:[1,0,1]
	ds_read_b128 v[236:239], v244 offset:39936
	s_waitcnt lgkmcnt(3)
	v_pk_fma_f32 v[180:181], v[92:93], v[224:225], v[180:181] op_sel_hi:[1,0,1]
	s_nop 0
	v_pk_fma_f32 v[176:177], v[94:95], v[224:225], v[180:181] op_sel:[0,1,0]
	s_nop 0
	v_pk_fma_f32 v[176:177], v[100:101], v[226:227], v[176:177] op_sel_hi:[1,0,1]
	v_mov_b32_e32 v178, v227
	v_pk_fma_f32 v[180:181], v[104:105], v[178:179], v[176:177] op_sel_hi:[1,0,1]
	ds_read_b128 v[240:243], v244 offset:40960
	s_waitcnt lgkmcnt(3)
	v_pk_fma_f32 v[180:181], v[80:81], v[228:229], v[180:181] op_sel_hi:[1,0,1]
	s_nop 0
	v_pk_fma_f32 v[176:177], v[82:83], v[228:229], v[180:181] op_sel:[0,1,0]
	s_nop 0
	v_pk_fma_f32 v[176:177], v[86:87], v[230:231], v[176:177] op_sel_hi:[1,0,1]
	v_mov_b32_e32 v178, v231
	v_pk_fma_f32 v[180:181], v[90:91], v[178:179], v[176:177] op_sel_hi:[1,0,1]
	ds_read_b128 v[224:227], v244 offset:41984
	s_waitcnt lgkmcnt(3)
	v_pk_fma_f32 v[180:181], v[76:77], v[232:233], v[180:181] op_sel_hi:[1,0,1]
	s_nop 0
	v_pk_fma_f32 v[176:177], v[78:79], v[232:233], v[180:181] op_sel:[0,1,0]
	s_nop 0
	v_pk_fma_f32 v[176:177], v[84:85], v[234:235], v[176:177] op_sel_hi:[1,0,1]
	v_mov_b32_e32 v178, v235
	v_pk_fma_f32 v[180:181], v[88:89], v[178:179], v[176:177] op_sel_hi:[1,0,1]
	ds_read_b128 v[228:231], v244 offset:43008
	s_waitcnt lgkmcnt(3)
	v_pk_fma_f32 v[180:181], v[68:69], v[236:237], v[180:181] op_sel_hi:[1,0,1]
	s_nop 0
	v_pk_fma_f32 v[176:177], v[70:71], v[236:237], v[180:181] op_sel:[0,1,0]
	s_nop 0
	v_pk_fma_f32 v[176:177], v[72:73], v[238:239], v[176:177] op_sel_hi:[1,0,1]
	v_mov_b32_e32 v178, v239
	v_pk_fma_f32 v[176:177], v[74:75], v[178:179], v[176:177] op_sel_hi:[1,0,1]
	ds_read_b128 v[232:235], v244 offset:44032
	s_waitcnt lgkmcnt(3)
	v_pk_fma_f32 v[184:185], v[124:125], v[240:241], 0 op_sel_hi:[1,0,0]
	s_nop 0
	v_pk_fma_f32 v[178:179], v[126:127], v[240:241], v[184:185] op_sel:[0,1,0]
	s_nop 0
	v_pk_fma_f32 v[178:179], v[128:129], v[242:243], v[178:179] op_sel_hi:[1,0,1]
	v_mov_b32_e32 v180, v243
	v_pk_fma_f32 v[184:185], v[130:131], v[180:181], v[178:179] op_sel_hi:[1,0,1]
	ds_read_b128 v[236:239], v244 offset:45056
	s_waitcnt lgkmcnt(3)
	v_pk_fma_f32 v[184:185], v[112:113], v[224:225], v[184:185] op_sel_hi:[1,0,1]
	s_nop 0
	v_pk_fma_f32 v[178:179], v[114:115], v[224:225], v[184:185] op_sel:[0,1,0]
	s_nop 0
	v_pk_fma_f32 v[178:179], v[118:119], v[226:227], v[178:179] op_sel_hi:[1,0,1]
	v_mov_b32_e32 v180, v227
	v_pk_fma_f32 v[184:185], v[122:123], v[180:181], v[178:179] op_sel_hi:[1,0,1]
	ds_read_b128 v[240:243], v244 offset:46080
	s_waitcnt lgkmcnt(3)
	v_pk_fma_f32 v[184:185], v[108:109], v[228:229], v[184:185] op_sel_hi:[1,0,1]
	s_nop 0
	v_pk_fma_f32 v[178:179], v[110:111], v[228:229], v[184:185] op_sel:[0,1,0]
	s_nop 0
	v_pk_fma_f32 v[178:179], v[116:117], v[230:231], v[178:179] op_sel_hi:[1,0,1]
	v_mov_b32_e32 v180, v231
	v_pk_fma_f32 v[184:185], v[120:121], v[180:181], v[178:179] op_sel_hi:[1,0,1]
	ds_read_b128 v[224:227], v244 offset:47104
	s_waitcnt lgkmcnt(3)
	v_pk_fma_f32 v[184:185], v[96:97], v[232:233], v[184:185] op_sel_hi:[1,0,1]
	s_nop 0
	v_pk_fma_f32 v[178:179], v[98:99], v[232:233], v[184:185] op_sel:[0,1,0]
	s_nop 0
	v_pk_fma_f32 v[178:179], v[102:103], v[234:235], v[178:179] op_sel_hi:[1,0,1]
	v_mov_b32_e32 v180, v235
	v_pk_fma_f32 v[184:185], v[106:107], v[180:181], v[178:179] op_sel_hi:[1,0,1]
	ds_read_b128 v[228:231], v244 offset:48128
	s_waitcnt lgkmcnt(3)
; #define LAS __attribute__((address_space(3)))
; __device__ __forceinline__ void phase_norm2(const Params& p, const Ctx& F, const int l) {
;     ...
; #pragma unroll
;         for (int e = 0; e < 16; ++e) { f32x2 a = {0.f, 0.f};
; #pragma unroll
;             for (int j = 0; j < 8; ++j) { const f32x4 w = *((const LAS f32x4*)(wr2 + e * DM) + F.lane + 64 * j);
; #pragma unroll
;                 for (int c = 0; c < 4; ++c) a += vv[j][c] * w[c]; }
;             lg[e] = a; }
	v_pk_fma_f32 v[184:185], v[92:93], v[236:237], v[184:185] op_sel_hi:[1,0,1]
	s_nop 0
	v_pk_fma_f32 v[178:179], v[94:95], v[236:237], v[184:185] op_sel:[0,1,0]
	s_nop 0
	v_pk_fma_f32 v[178:179], v[100:101], v[238:239], v[178:179] op_sel_hi:[1,0,1]
	v_mov_b32_e32 v180, v239
	v_pk_fma_f32 v[184:185], v[104:105], v[180:181], v[178:179] op_sel_hi:[1,0,1]
	ds_read_b128 v[232:235], v244 offset:49152
	s_waitcnt lgkmcnt(3)
	v_pk_fma_f32 v[184:185], v[80:81], v[240:241], v[184:185] op_sel_hi:[1,0,1]
	s_nop 0
	v_pk_fma_f32 v[178:179], v[82:83], v[240:241], v[184:185] op_sel:[0,1,0]
	s_nop 0
	v_pk_fma_f32 v[178:179], v[86:87], v[242:243], v[178:179] op_sel_hi:[1,0,1]
	v_mov_b32_e32 v180, v243
	v_pk_fma_f32 v[184:185], v[90:91], v[180:181], v[178:179] op_sel_hi:[1,0,1]
	ds_read_b128 v[236:239], v244 offset:50176
	s_waitcnt lgkmcnt(3)
	v_pk_fma_f32 v[184:185], v[76:77], v[224:225], v[184:185] op_sel_hi:[1,0,1]
	s_nop 0
	v_pk_fma_f32 v[178:179], v[78:79], v[224:225], v[184:185] op_sel:[0,1,0]
	s_nop 0
	v_pk_fma_f32 v[178:179], v[84:85], v[226:227], v[178:179] op_sel_hi:[1,0,1]
	v_mov_b32_e32 v180, v227
	v_pk_fma_f32 v[184:185], v[88:89], v[180:181], v[178:179] op_sel_hi:[1,0,1]
	ds_read_b128 v[240:243], v244 offset:51200
	s_waitcnt lgkmcnt(3)
	v_pk_fma_f32 v[184:185], v[68:69], v[228:229], v[184:185] op_sel_hi:[1,0,1]
	s_nop 0
	v_pk_fma_f32 v[178:179], v[70:71], v[228:229], v[184:185] op_sel:[0,1,0]
	ds_read_b128 v[224:227], v244 offset:52224
	v_pk_fma_f32 v[178:179], v[72:73], v[230:231], v[178:179] op_sel_hi:[1,0,1]
	v_mov_b32_e32 v180, v231
	v_pk_fma_f32 v[178:179], v[74:75], v[180:181], v[178:179] op_sel_hi:[1,0,1]
	s_waitcnt lgkmcnt(3)
	v_pk_fma_f32 v[180:181], v[124:125], v[232:233], 0 op_sel_hi:[1,0,0]
	s_nop 0
	v_pk_fma_f32 v[180:181], v[126:127], v[232:233], v[180:181] op_sel:[0,1,0]
	v_mov_b32_e32 v184, v235
	v_pk_fma_f32 v[180:181], v[128:129], v[234:235], v[180:181] op_sel_hi:[1,0,1]
	s_nop 0
	v_pk_fma_f32 v[180:181], v[130:131], v[184:185], v[180:181] op_sel_hi:[1,0,1]
	ds_read_b128 v[228:231], v244 offset:53248
	s_waitcnt lgkmcnt(3)
	v_pk_fma_f32 v[180:181], v[112:113], v[236:237], v[180:181] op_sel_hi:[1,0,1]
	s_nop 0
	v_pk_fma_f32 v[180:181], v[114:115], v[236:237], v[180:181] op_sel:[0,1,0]
	v_mov_b32_e32 v184, v239
	v_pk_fma_f32 v[180:181], v[118:119], v[238:239], v[180:181] op_sel_hi:[1,0,1]
	s_nop 0
	v_pk_fma_f32 v[180:181], v[122:123], v[184:185], v[180:181] op_sel_hi:[1,0,1]
	ds_read_b128 v[232:235], v244 offset:54272
	s_waitcnt lgkmcnt(3)
	v_pk_fma_f32 v[180:181], v[108:109], v[240:241], v[180:181] op_sel_hi:[1,0,1]
	s_nop 0
	v_pk_fma_f32 v[180:181], v[110:111], v[240:241], v[180:181] op_sel:[0,1,0]
	v_mov_b32_e32 v184, v243
	v_pk_fma_f32 v[180:181], v[116:117], v[242:243], v[180:181] op_sel_hi:[1,0,1]
	s_nop 0
	v_pk_fma_f32 v[180:181], v[120:121], v[184:185], v[180:181] op_sel_hi:[1,0,1]
	ds_read_b128 v[236:239], v244 offset:55296
	s_waitcnt lgkmcnt(3)
	v_pk_fma_f32 v[180:181], v[96:97], v[224:225], v[180:181] op_sel_hi:[1,0,1]
	s_nop 0
	v_pk_fma_f32 v[180:181], v[98:99], v[224:225], v[180:181] op_sel:[0,1,0]
	v_mov_b32_e32 v184, v227
	v_pk_fma_f32 v[180:181], v[102:103], v[226:227], v[180:181] op_sel_hi:[1,0,1]
	s_nop 0
	v_pk_fma_f32 v[180:181], v[106:107], v[184:185], v[180:181] op_sel_hi:[1,0,1]
	ds_read_b128 v[240:243], v244 offset:56320
	s_waitcnt lgkmcnt(3)
	v_pk_fma_f32 v[180:181], v[92:93], v[228:229], v[180:181] op_sel_hi:[1,0,1]
	s_nop 0
	v_pk_fma_f32 v[180:181], v[94:95], v[228:229], v[180:181] op_sel:[0,1,0]
	v_mov_b32_e32 v184, v231
	v_pk_fma_f32 v[180:181], v[100:101], v[230:231], v[180:181] op_sel_hi:[1,0,1]
	s_nop 0
	v_pk_fma_f32 v[180:181], v[104:105], v[184:185], v[180:181] op_sel_hi:[1,0,1]
	ds_read_b128 v[224:227], v244 offset:57344
	s_waitcnt lgkmcnt(3)
	v_pk_fma_f32 v[180:181], v[80:81], v[232:233], v[180:181] op_sel_hi:[1,0,1]
	s_nop 0
	v_pk_fma_f32 v[180:181], v[82:83], v[232:233], v[180:181] op_sel:[0,1,0]
	v_mov_b32_e32 v184, v235
	v_pk_fma_f32 v[180:181], v[86:87], v[234:235], v[180:181] op_sel_hi:[1,0,1]
	s_nop 0
	v_pk_fma_f32 v[180:181], v[90:91], v[184:185], v[180:181] op_sel_hi:[1,0,1]
	ds_read_b128 v[228:231], v244 offset:58368
	s_waitcnt lgkmcnt(3)
	v_pk_fma_f32 v[180:181], v[76:77], v[236:237], v[180:181] op_sel_hi:[1,0,1]
	s_nop 0
	v_pk_fma_f32 v[180:181], v[78:79], v[236:237], v[180:181] op_sel:[0,1,0]
	v_mov_b32_e32 v184, v239
	v_pk_fma_f32 v[180:181], v[84:85], v[238:239], v[180:181] op_sel_hi:[1,0,1]
	s_nop 0
	v_pk_fma_f32 v[180:181], v[88:89], v[184:185], v[180:181] op_sel_hi:[1,0,1]
	ds_read_b128 v[232:235], v244 offset:59392
	s_waitcnt lgkmcnt(3)
	v_pk_fma_f32 v[180:181], v[68:69], v[240:241], v[180:181] op_sel_hi:[1,0,1]
	s_nop 0
	v_pk_fma_f32 v[180:181], v[70:71], v[240:241], v[180:181] op_sel:[0,1,0]
	v_mov_b32_e32 v184, v243
	v_pk_fma_f32 v[180:181], v[72:73], v[242:243], v[180:181] op_sel_hi:[1,0,1]
	s_nop 0
	v_pk_fma_f32 v[180:181], v[74:75], v[184:185], v[180:181] op_sel_hi:[1,0,1]
	ds_read_b128 v[236:239], v244 offset:60416
	s_waitcnt lgkmcnt(3)
	v_pk_fma_f32 v[124:125], v[124:125], v[224:225], 0 op_sel_hi:[1,0,0]
	s_nop 0
	v_pk_fma_f32 v[124:125], v[126:127], v[224:225], v[124:125] op_sel:[0,1,0]
	v_mov_b32_e32 v126, v227
	v_pk_fma_f32 v[124:125], v[128:129], v[226:227], v[124:125] op_sel_hi:[1,0,1]
	s_nop 0
	v_pk_fma_f32 v[128:129], v[130:131], v[126:127], v[124:125] op_sel_hi:[1,0,1]
	ds_read_b128 v[240:243], v244 offset:61440
	s_waitcnt lgkmcnt(3)
	v_pk_fma_f32 v[112:113], v[112:113], v[228:229], v[128:129] op_sel_hi:[1,0,1]
	s_nop 0
	v_pk_fma_f32 v[112:113], v[114:115], v[228:229], v[112:113] op_sel:[0,1,0]
	v_mov_b32_e32 v114, v231
	v_pk_fma_f32 v[112:113], v[118:119], v[230:231], v[112:113] op_sel_hi:[1,0,1]
	s_nop 0
	v_pk_fma_f32 v[118:119], v[122:123], v[114:115], v[112:113] op_sel_hi:[1,0,1]
	ds_read_b128 v[224:227], v244 offset:62464
	s_waitcnt lgkmcnt(3)
; #define LAS __attribute__((address_space(3)))
; __device__ __forceinline__ void router_tail(const Ctx& F, const float (&lg)[16], const int b, const int t, const bool valid) {
;     const bool b5 = (F.lane & 32) != 0, b4 = (F.lane & 16) != 0, b3 = (F.lane & 8) != 0, b2 = (F.lane & 4) != 0;
;     float r8[8], r4[4], r2[2];
; #pragma unroll
;     for (int e = 0; e < 8; ++e) { const float keep = b5 ? lg[e + 8] : lg[e], send = b5 ? lg[e] : lg[e + 8]; r8[e] = keep + __shfl_xor(send, 32); }
; #pragma unroll
;     for (int e = 0; e < 4; ++e) { const float keep = b4 ? r8[e + 4] : r8[e], send = b4 ? r8[e] : r8[e + 4]; r4[e] = keep + __shfl_xor(send, 16); }
; #pragma unroll
;     for (int e = 0; e < 2; ++e) { const float keep = b3 ? r4[e + 2] : r4[e], send = b3 ? r4[e] : r4[e + 2]; r2[e] = keep + __shfl_xor(send, 8); }
;     float lgt; { const float keep = b2 ? r2[1] : r2[0], send = b2 ? r2[0] : r2[1]; lgt = keep + __shfl_xor(send, 4); }
;     lgt += __shfl_xor(lgt, 2); lgt += __shfl_xor(lgt, 1);
;     float mx = lgt;
;     mx = fmaxf(mx, __shfl_xor(mx, 4)); mx = fmaxf(mx, __shfl_xor(mx, 8)); mx = fmaxf(mx, __shfl_xor(mx, 16)); mx = fmaxf(mx, __shfl_xor(mx, 32));
;     const float ex = expf(lgt - mx); float sum = ex;
;     sum += __shfl_xor(sum, 4); sum += __shfl_xor(sum, 8); sum += __shfl_xor(sum, 16); sum += __shfl_xor(sum, 32);
;     if (valid && (F.lane & 3) == 0) { const float af = ex / sum; const int e = F.lane >> 2;
;         if (t < CTXL) F.affc[((size_t)(b * 16 + e)) * CTXL + t] = af; else F.affl[((size_t)(b * 16 + e)) * SEQ + (t - CTXL)] = af; }
; __device__ __forceinline__ void phase_norm2(const Params& p, const Ctx& F, const int l) {
;     ...
; #pragma unroll
;         for (int e = 0; e < 16; ++e) { f32x2 a = {0.f, 0.f};
; #pragma unroll
;             for (int j = 0; j < 8; ++j) { const f32x4 w = *((const LAS f32x4*)(wr2 + e * DM) + F.lane + 64 * j);
; #pragma unroll
;                 for (int c = 0; c < 4; ++c) a += vv[j][c] * w[c]; }
;             lg[e] = a; }
	v_pk_fma_f32 v[108:109], v[108:109], v[232:233], v[118:119] op_sel_hi:[1,0,1]
	s_nop 0
	v_pk_fma_f32 v[108:109], v[110:111], v[232:233], v[108:109] op_sel:[0,1,0]
	v_mov_b32_e32 v110, v235
	v_pk_fma_f32 v[108:109], v[116:117], v[234:235], v[108:109] op_sel_hi:[1,0,1]
	s_nop 0
	v_pk_fma_f32 v[112:113], v[120:121], v[110:111], v[108:109] op_sel_hi:[1,0,1]
	ds_read_b128 v[228:231], v244 offset:63488
	s_waitcnt lgkmcnt(3)
	v_pk_fma_f32 v[96:97], v[96:97], v[236:237], v[112:113] op_sel_hi:[1,0,1]
	s_nop 0
	v_pk_fma_f32 v[96:97], v[98:99], v[236:237], v[96:97] op_sel:[0,1,0]
	v_mov_b32_e32 v98, v239
	v_pk_fma_f32 v[96:97], v[102:103], v[238:239], v[96:97] op_sel_hi:[1,0,1]
	s_nop 0
	v_pk_fma_f32 v[102:103], v[106:107], v[98:99], v[96:97] op_sel_hi:[1,0,1]
	ds_read_b128 v[232:235], v244 offset:64512
	s_waitcnt lgkmcnt(3)
	v_pk_fma_f32 v[92:93], v[92:93], v[240:241], v[102:103] op_sel_hi:[1,0,1]
	s_nop 0
	v_pk_fma_f32 v[92:93], v[94:95], v[240:241], v[92:93] op_sel:[0,1,0]
	v_mov_b32_e32 v94, v243
	v_pk_fma_f32 v[92:93], v[100:101], v[242:243], v[92:93] op_sel_hi:[1,0,1]
	s_nop 0
	v_pk_fma_f32 v[96:97], v[104:105], v[94:95], v[92:93] op_sel_hi:[1,0,1]
	s_waitcnt lgkmcnt(2)
	v_pk_fma_f32 v[80:81], v[80:81], v[224:225], v[96:97] op_sel_hi:[1,0,1]
	s_nop 0
	v_pk_fma_f32 v[80:81], v[82:83], v[224:225], v[80:81] op_sel:[0,1,0]
	v_mov_b32_e32 v82, v227
	v_pk_fma_f32 v[80:81], v[86:87], v[226:227], v[80:81] op_sel_hi:[1,0,1]
	s_nop 0
	v_pk_fma_f32 v[86:87], v[90:91], v[82:83], v[80:81] op_sel_hi:[1,0,1]
	s_waitcnt lgkmcnt(1)
	v_pk_fma_f32 v[76:77], v[76:77], v[228:229], v[86:87] op_sel_hi:[1,0,1]
	s_nop 0
	v_pk_fma_f32 v[76:77], v[78:79], v[228:229], v[76:77] op_sel:[0,1,0]
	v_mov_b32_e32 v78, v231
	v_pk_fma_f32 v[76:77], v[84:85], v[230:231], v[76:77] op_sel_hi:[1,0,1]
	s_nop 0
	v_pk_fma_f32 v[80:81], v[88:89], v[78:79], v[76:77] op_sel_hi:[1,0,1]
	v_cndmask_b32_e64 v1, v168, v152, s[38:39]
	s_waitcnt lgkmcnt(0)
	v_pk_fma_f32 v[68:69], v[68:69], v[232:233], v[80:81] op_sel_hi:[1,0,1]
	s_nop 0
	v_pk_fma_f32 v[68:69], v[70:71], v[232:233], v[68:69] op_sel:[0,1,0]
	v_mov_b32_e32 v70, v235
	v_pk_fma_f32 v[68:69], v[72:73], v[234:235], v[68:69] op_sel_hi:[1,0,1]
	v_cndmask_b32_e64 v72, v156, v172, s[38:39]
	v_pk_fma_f32 v[68:69], v[74:75], v[70:71], v[68:69] op_sel_hi:[1,0,1]
	s_nop 1
	v_permlane32_swap_b32_e32 v152, v168
	v_permlane32_swap_b32_e32 v154, v170
	v_permlane32_swap_b32_e32 v156, v172
	v_permlane32_swap_b32_e32 v158, v174
	v_permlane32_swap_b32_e32 v160, v176
	v_permlane32_swap_b32_e32 v162, v178
	v_permlane32_swap_b32_e32 v164, v180
	v_permlane32_swap_b32_e32 v166, v68
	v_add_f32_e32 v1, v152, v168
	v_add_f32_e32 v70, v154, v170
	v_add_f32_e32 v71, v156, v172
	v_add_f32_e32 v72, v158, v174
	v_add_f32_e32 v73, v160, v176
	v_add_f32_e32 v74, v162, v178
	v_add_f32_e32 v75, v164, v180
	v_add_f32_e32 v68, v166, v68
	s_waitcnt lgkmcnt(0)
	s_nop 1
	v_permlane16_swap_b32_e32 v1, v73
	v_permlane16_swap_b32_e32 v70, v74
	v_permlane16_swap_b32_e32 v71, v75
	v_permlane16_swap_b32_e32 v72, v68
	v_add_f32_e32 v1, v1, v73
	v_add_f32_e32 v70, v70, v74
	v_add_f32_e32 v71, v71, v75
	v_add_f32_e32 v68, v72, v68
	v_cndmask_b32_e64 v72, v71, v1, s[42:43]
	v_cndmask_b32_e64 v1, v1, v71, s[42:43]
	v_cndmask_b32_e64 v71, v68, v70, s[42:43]
	v_cndmask_b32_e64 v68, v70, v68, s[42:43]
	s_nop 1
	v_add_f32_dpp v1, v1, v72 row_ror:8 row_mask:0xf bank_mask:0xf
	v_add_f32_dpp v68, v68, v71 row_ror:8 row_mask:0xf bank_mask:0xf
	v_cndmask_b32_e64 v70, v68, v1, s[4:5]
	v_cndmask_b32_e64 v1, v1, v68, s[4:5]
	ds_bpermute_b32 v1, v191, v1
	s_waitcnt lgkmcnt(0)
	v_add_f32_e32 v1, v70, v1
	s_nop 1
	v_add_f32_dpp v1, v1, v1 quad_perm:[2,3,0,1] row_mask:0xf bank_mask:0xf
	s_nop 1
	v_add_f32_dpp v1, v1, v1 quad_perm:[1,0,3,2] row_mask:0xf bank_mask:0xf
	s_nop 1
	v_max_f32_dpp v68, v1, v1 row_half_mirror row_mask:0xf bank_mask:0xf
	s_nop 1
	v_max_f32_dpp v68, v68, v68 row_mirror row_mask:0xf bank_mask:0xf
	v_mov_b32_e32 v70, v68
	s_nop 1
	v_permlane16_swap_b32_e32 v68, v70
	v_max_f32_e32 v68, v68, v70
	v_mov_b32_e32 v70, v68
	s_nop 1
	v_permlane32_swap_b32_e32 v68, v70
	v_max_f32_e32 v68, v68, v70
	v_sub_f32_e32 v1, v1, v68
	v_mul_f32_e32 v68, 0x3fb8aa3b, v1
	v_fma_f32 v70, v1, s55, -v68
	v_rndne_f32_e32 v71, v68
	v_fmac_f32_e32 v70, 0x32a5705f, v1
	v_sub_f32_e32 v68, v68, v71
	v_add_f32_e32 v68, v68, v70
	v_exp_f32_e32 v68, v68
	v_cvt_i32_f32_e32 v70, v71
	v_cmp_ngt_f32_e32 vcc, s56, v1
	v_ldexp_f32 v68, v68, v70
	s_nop 0
	v_cndmask_b32_e32 v68, 0, v68, vcc
	v_cmp_nlt_f32_e32 vcc, s57, v1
	s_nop 1
	v_cndmask_b32_e32 v68, v222, v68, vcc
	s_nop 1
	v_add_f32_dpp v1, v68, v68 row_half_mirror row_mask:0xf bank_mask:0xf
	s_nop 1
	v_add_f32_dpp v1, v1, v1 row_mirror row_mask:0xf bank_mask:0xf
	v_mov_b32_e32 v70, v1
	s_nop 1
	v_permlane16_swap_b32_e32 v1, v70
	v_add_f32_e32 v70, v1, v70
	ds_bpermute_b32 v71, v194, v70
	s_and_saveexec_b64 s[0:1], s[6:7]
	s_cbranch_execz .LBB0_942
	s_waitcnt lgkmcnt(0)
	v_add_f32_e32 v1, v70, v71
	v_div_scale_f32 v70, s[12:13], v1, v1, v68
	v_rcp_f32_e32 v71, v70
	v_div_scale_f32 v72, vcc, v68, v1, v68
	s_cmpk_gt_i32 s60, 0xff
	v_fma_f32 v73, -v70, v71, 1.0
	v_fmac_f32_e32 v71, v73, v71
	v_mul_f32_e32 v73, v72, v71
	v_fma_f32 v74, -v70, v73, v72
	v_fmac_f32_e32 v73, v74, v71
	v_fma_f32 v70, -v70, v73, v72
	v_div_fmas_f32 v70, v70, v71, v73
	v_div_fixup_f32 v68, v70, v1, v68
	s_mov_b64 s[12:13], -1
	s_cbranch_scc0 .LBB0_940
	v_lshl_add_u64 v[70:71], s[60:61], 2, v[148:149]
	global_store_dword v[70:71], v68, off offset:-1024
	s_mov_b64 s[12:13], 0

; __device__ __forceinline__ void router_tail(const Ctx& F, const float (&lg)[16], const int b, const int t, const bool valid) {
;     const bool b5 = (F.lane & 32) != 0, b4 = (F.lane & 16) != 0, b3 = (F.lane & 8) != 0, b2 = (F.lane & 4) != 0;
;     float r8[8], r4[4], r2[2];
; #pragma unroll
;     for (int e = 0; e < 8; ++e) { const float keep = b5 ? lg[e + 8] : lg[e], send = b5 ? lg[e] : lg[e + 8]; r8[e] = keep + __shfl_xor(send, 32); }
; #pragma unroll
;     for (int e = 0; e < 4; ++e) { const float keep = b4 ? r8[e + 4] : r8[e], send = b4 ? r8[e] : r8[e + 4]; r4[e] = keep + __shfl_xor(send, 16); }
; #pragma unroll
;     for (int e = 0; e < 2; ++e) { const float keep = b3 ? r4[e + 2] : r4[e], send = b3 ? r4[e] : r4[e + 2]; r2[e] = keep + __shfl_xor(send, 8); }
;     float lgt; { const float keep = b2 ? r2[1] : r2[0], send = b2 ? r2[0] : r2[1]; lgt = keep + __shfl_xor(send, 4); }
;     lgt += __shfl_xor(lgt, 2); lgt += __shfl_xor(lgt, 1);
;     float mx = lgt;
;     mx = fmaxf(mx, __shfl_xor(mx, 4)); mx = fmaxf(mx, __shfl_xor(mx, 8)); mx = fmaxf(mx, __shfl_xor(mx, 16)); mx = fmaxf(mx, __shfl_xor(mx, 32));
;     const float ex = expf(lgt - mx); float sum = ex;
;     sum += __shfl_xor(sum, 4); sum += __shfl_xor(sum, 8); sum += __shfl_xor(sum, 16); sum += __shfl_xor(sum, 32);
;     if (valid && (F.lane & 3) == 0) { const float af = ex / sum; const int e = F.lane >> 2;
;         if (t < CTXL) F.affc[((size_t)(b * 16 + e)) * CTXL + t] = af; else F.affl[((size_t)(b * 16 + e)) * SEQ + (t - CTXL)] = af; }
.LBB0_942:
	s_or_b64 exec, exec, s[0:1]
	s_and_b64 s[8:9], s[6:7], s[8:9]
	s_waitcnt lgkmcnt(0)
	s_nop 1
	v_permlane32_swap_b32_e32 v153, v169
	v_permlane32_swap_b32_e32 v155, v171
	v_permlane32_swap_b32_e32 v157, v173
	v_permlane32_swap_b32_e32 v159, v175
	v_permlane32_swap_b32_e32 v161, v177
	v_permlane32_swap_b32_e32 v163, v179
	v_permlane32_swap_b32_e32 v165, v181
	v_permlane32_swap_b32_e32 v167, v69
	v_add_f32_e32 v1, v153, v169
	v_add_f32_e32 v68, v155, v171
	v_add_f32_e32 v70, v157, v173
	v_add_f32_e32 v71, v159, v175
	v_add_f32_e32 v72, v161, v177
	v_add_f32_e32 v73, v163, v179
	v_add_f32_e32 v74, v165, v181
	v_add_f32_e32 v69, v167, v69
	s_waitcnt lgkmcnt(0)
	s_nop 1
	v_permlane16_swap_b32_e32 v1, v72
	v_permlane16_swap_b32_e32 v68, v73
	v_permlane16_swap_b32_e32 v70, v74
	v_permlane16_swap_b32_e32 v71, v69
	v_add_f32_e32 v1, v1, v72
	v_add_f32_e32 v68, v68, v73
	v_add_f32_e32 v70, v70, v74
	v_add_f32_e32 v69, v71, v69
	v_cndmask_b32_e64 v71, v70, v1, s[42:43]
	v_cndmask_b32_e64 v1, v1, v70, s[42:43]
	v_cndmask_b32_e64 v70, v69, v68, s[42:43]
	v_cndmask_b32_e64 v68, v68, v69, s[42:43]
	s_nop 1
	v_add_f32_dpp v1, v1, v71 row_ror:8 row_mask:0xf bank_mask:0xf
	v_add_f32_dpp v68, v68, v70 row_ror:8 row_mask:0xf bank_mask:0xf
	v_cndmask_b32_e64 v69, v68, v1, s[4:5]
	v_cndmask_b32_e64 v1, v1, v68, s[4:5]
	ds_bpermute_b32 v1, v191, v1
	s_waitcnt lgkmcnt(0)
	v_add_f32_e32 v1, v69, v1
	s_nop 1
	v_add_f32_dpp v1, v1, v1 quad_perm:[2,3,0,1] row_mask:0xf bank_mask:0xf
	s_nop 1
	v_add_f32_dpp v1, v1, v1 quad_perm:[1,0,3,2] row_mask:0xf bank_mask:0xf
	s_nop 1
	v_max_f32_dpp v68, v1, v1 row_half_mirror row_mask:0xf bank_mask:0xf
	s_nop 1
	v_max_f32_dpp v68, v68, v68 row_mirror row_mask:0xf bank_mask:0xf
	v_mov_b32_e32 v69, v68
	s_nop 1
	v_permlane16_swap_b32_e32 v68, v69
	v_max_f32_e32 v68, v68, v69
	v_mov_b32_e32 v69, v68
	s_nop 1
	v_permlane32_swap_b32_e32 v68, v69
	v_max_f32_e32 v68, v68, v69
	v_sub_f32_e32 v1, v1, v68
	v_mul_f32_e32 v68, 0x3fb8aa3b, v1
	v_fma_f32 v69, v1, s55, -v68
	v_rndne_f32_e32 v70, v68
	v_fmac_f32_e32 v69, 0x32a5705f, v1
	v_sub_f32_e32 v68, v68, v70
	v_add_f32_e32 v68, v68, v69
	v_exp_f32_e32 v68, v68
	v_cvt_i32_f32_e32 v69, v70
	v_cmp_ngt_f32_e32 vcc, s56, v1
	v_ldexp_f32 v68, v68, v69
	s_nop 0
	v_cndmask_b32_e32 v68, 0, v68, vcc
	v_cmp_nlt_f32_e32 vcc, s57, v1
	s_nop 1
	v_cndmask_b32_e32 v68, v222, v68, vcc
	s_nop 1
	v_add_f32_dpp v1, v68, v68 row_half_mirror row_mask:0xf bank_mask:0xf
	s_nop 1
	v_add_f32_dpp v1, v1, v1 row_mirror row_mask:0xf bank_mask:0xf
	v_mov_b32_e32 v69, v1
	s_nop 1
	v_permlane16_swap_b32_e32 v1, v69
	v_add_f32_e32 v69, v1, v69
	ds_bpermute_b32 v70, v194, v69
	s_and_saveexec_b64 s[0:1], s[8:9]
	s_cbranch_execz .LBB0_911
	s_waitcnt lgkmcnt(0)
	v_add_f32_e32 v1, v69, v70
	v_div_scale_f32 v69, s[8:9], v1, v1, v68
	v_rcp_f32_e32 v70, v69
	v_div_scale_f32 v71, vcc, v68, v1, v68
	s_cmpk_gt_i32 s2, 0xff
	v_fma_f32 v72, -v69, v70, 1.0
	v_fmac_f32_e32 v70, v72, v70
	v_mul_f32_e32 v72, v71, v70
	v_fma_f32 v73, -v69, v72, v71
	v_fmac_f32_e32 v72, v73, v70
	v_fma_f32 v69, -v69, v72, v71
	v_div_fmas_f32 v69, v69, v70, v72
	v_div_fixup_f32 v68, v69, v1, v68
	s_mov_b64 s[8:9], -1
	s_cbranch_scc0 .LBB0_945
	s_mov_b32 s3, s61
	v_lshl_add_u64 v[70:71], s[2:3], 2, v[148:149]
	global_store_dword v[70:71], v68, off offset:-1024
	s_mov_b64 s[8:9], 0
